# speedup vs baseline: 1.0061x; 1.0061x over previous
.Lmy_loopb:
	ds_read_b128 v[158:161], v248 offset:0
	ds_read_b128 v[162:165], v248 offset:1024
	ds_read_b128 v[166:169], v249 offset:2048
	ds_read_b128 v[170:173], v249 offset:3072
	v_mfma_f32_16x16x32_f16 v[218:221], v[82:85], v[150:153], v[106:109]
	v_mfma_f32_16x16x32_f16 v[222:225], v[90:93], v[150:153], v[110:113]
	v_mfma_f32_16x16x32_f16 v[218:221], v[86:89], v[154:157], v[218:221]
	v_mfma_f32_16x16x32_f16 v[222:225], v[94:97], v[154:157], v[222:225]
	s_waitcnt lgkmcnt(2)
	v_mfma_f32_16x16x32_f16 v[210:213], v[54:57], v[158:161], v[210:213]
	v_mfma_f32_16x16x32_f16 v[210:213], v[58:61], v[162:165], v[210:213]
	s_waitcnt lgkmcnt(0)
	v_mfma_f32_16x16x32_f16 v[210:213], v[62:65], v[166:169], v[210:213]
	v_mfma_f32_16x16x32_f16 v[210:213], v[50:53], v[170:173], v[210:213]
	s_waitcnt vmcnt(9)
	v_cvt_pk_f16_f32 v251, v192, v193
	ds_write_b32 v1, v251 offset:0
	ds_read_b128 v[150:153], v186 offset:6144
	ds_read_b128 v[154:157], v186 offset:7168
	s_nop 2
	v_exp_f32_e32 v226, v210
	v_exp_f32_e32 v227, v211
	v_mfma_f32_16x16x32_f16 v[214:217], v[34:37], v[158:161], v[214:217]
	v_min_f32_e32 v228, s42, v212
	v_exp_f32_e32 v229, v213
	v_mfma_f32_16x16x32_f16 v[214:217], v[38:41], v[162:165], v[214:217]
	v_exp_f32_e32 v228, v228
	v_add_f32_e32 v227, 1.0, v227
	v_mfma_f32_16x16x32_f16 v[214:217], v[42:45], v[166:169], v[214:217]
	v_fma_f32 v230, v228, s41, s41
	v_rcp_f32_e32 v227, v227
	v_mfma_f32_16x16x32_f16 v[214:217], v[46:49], v[170:173], v[214:217]
	v_fma_f32 v230, v226, v230, v230
	v_rcp_f32_e32 v230, v230
	v_mfma_f32_16x16x32_f16 v[218:221], v[18:21], v[158:161], v[218:221]
	v_fma_f32 v226, -v228, v230, v230
	v_fma_f32 v200, v200, v227, v226
	v_mfma_f32_16x16x32_f16 v[218:221], v[14:17], v[162:165], v[218:221]
	v_exp_f32_e32 v226, v200
	s_nop 0
	v_add_f32_e32 v227, 1.0, v226
	v_mfma_f32_16x16x32_f16 v[218:221], v[10:13], v[166:169], v[218:221]
	v_fma_f32 v227, v229, v227, v227
	v_rcp_f32_e32 v227, v227
	v_mfma_f32_16x16x32_f16 v[218:221], v[26:29], v[170:173], v[218:221]
	v_fma_f32 v226, -v226, v227, v227
	v_exp_f32_e32 v231, v214
	v_mfma_f32_16x16x32_f16 v[222:225], v[2:5], v[158:161], v[222:225]
	v_exp_f32_e32 v232, v215
	v_min_f32_e32 v233, s42, v216
	v_mfma_f32_16x16x32_f16 v[222:225], v[6:9], v[162:165], v[222:225]
	v_exp_f32_e32 v234, v217
	v_exp_f32_e32 v233, v233
	v_mfma_f32_16x16x32_f16 v[222:225], v[22:25], v[166:169], v[222:225]
	v_exp_f32_e32 v236, v218
	v_add_f32_e32 v232, 1.0, v232
	v_mfma_f32_16x16x32_f16 v[222:225], v[30:33], v[170:173], v[222:225]
	v_fma_f32 v235, v233, s41, s41
	v_exp_f32_e32 v227, v219
	v_rcp_f32_e32 v232, v232
	v_fma_f32 v235, v231, v235, v235
	v_min_f32_e32 v228, s42, v220
	v_rcp_f32_e32 v235, v235
	v_exp_f32_e32 v229, v221
	v_fma_f32 v231, -v233, v235, v235
	v_fma_f32 v201, v201, v232, v231
	v_exp_f32_e32 v231, v201
	v_exp_f32_e32 v228, v228
	v_add_f32_e32 v232, 1.0, v231
	v_fma_f32 v232, v234, v232, v232
	v_add_f32_e32 v227, 1.0, v227
	v_rcp_f32_e32 v232, v232
	v_mfma_f32_16x16x32_f16 v[146:149], v[122:125], v[158:161], v[146:149]
	v_fma_f32 v231, -v231, v232, v232
	v_fma_f32 v230, v228, s41, s41
	v_cvt_pk_f16_f32 v246, v226, v231
	v_mfma_f32_16x16x32_f16 v[146:149], v[126:129], v[162:165], v[146:149]
	v_exp_f32_e32 v231, v222
	v_rcp_f32_e32 v227, v227
	v_exp_f32_e32 v232, v223
	buffer_load_dwordx4 v[122:125], v189, s[76:79], s46 offen
	buffer_load_dwordx4 v[126:129], v208, s[76:79], s46 offen
	v_min_f32_e32 v233, s42, v224
	v_fma_f32 v230, v236, v230, v230
	v_exp_f32_e32 v234, v225
	s_waitcnt lgkmcnt(0)
	v_mfma_f32_16x16x32_f16 v[210:213], v[70:73], v[150:153], v[98:101]
	v_exp_f32_e32 v233, v233
	v_rcp_f32_e32 v230, v230
	v_add_f32_e32 v232, 1.0, v232
	v_mfma_f32_16x16x32_f16 v[214:217], v[74:77], v[150:153], v[102:105]
	v_fma_f32 v235, v233, s41, s41
	v_fma_f32 v236, -v228, v230, v230
	v_rcp_f32_e32 v232, v232
	v_fma_f32 v235, v231, v235, v235
	v_fma_f32 v198, v198, v227, v236
	v_rcp_f32_e32 v235, v235
	v_exp_f32_e32 v236, v198
	v_fma_f32 v231, -v233, v235, v235
	v_fma_f32 v199, v199, v232, v231
	v_exp_f32_e32 v231, v199
	v_add_f32_e32 v227, 1.0, v236
	v_add_f32_e32 v232, 1.0, v231
	v_fma_f32 v232, v234, v232, v232
	v_fma_f32 v227, v229, v227, v227
	v_rcp_f32_e32 v232, v232
	v_rcp_f32_e32 v227, v227
	v_fma_f32 v231, -v231, v232, v232
	v_fma_f32 v236, -v236, v227, v227
	v_cvt_pk_f16_f32 v247, v236, v231
	ds_write_b64 v250, v[246:247] offset:12288
	v_mfma_f32_16x16x32_f16 v[210:213], v[66:69], v[154:157], v[210:213]
	v_mfma_f32_16x16x32_f16 v[214:217], v[78:81], v[154:157], v[214:217]
	buffer_load_dwordx2 v[192:193], v209, s[56:59], s45 offen
	s_waitcnt lgkmcnt(0)
	s_barrier
	ds_read_b128 v[158:161], v248 offset:4096
	ds_read_b128 v[162:165], v248 offset:5120
	ds_read_b128 v[166:169], v249 offset:6144
	ds_read_b128 v[170:173], v249 offset:7168
	v_mfma_f32_16x16x32_f16 v[218:221], v[82:85], v[150:153], v[106:109]
	v_mfma_f32_16x16x32_f16 v[222:225], v[90:93], v[150:153], v[110:113]
	v_mfma_f32_16x16x32_f16 v[218:221], v[86:89], v[154:157], v[218:221]
	v_mfma_f32_16x16x32_f16 v[222:225], v[94:97], v[154:157], v[222:225]
	s_waitcnt lgkmcnt(2)
	v_mfma_f32_16x16x32_f16 v[210:213], v[54:57], v[158:161], v[210:213]
	v_mfma_f32_16x16x32_f16 v[210:213], v[58:61], v[162:165], v[210:213]
	s_waitcnt lgkmcnt(0)
	v_mfma_f32_16x16x32_f16 v[210:213], v[62:65], v[166:169], v[210:213]
	v_mfma_f32_16x16x32_f16 v[210:213], v[50:53], v[170:173], v[210:213]
	s_waitcnt vmcnt(9)
	v_cvt_pk_f16_f32 v251, v190, v191
	ds_write_b32 v1, v251 offset:2048
	ds_read_b128 v[150:153], v186 offset:0
	ds_read_b128 v[154:157], v186 offset:1024
	s_nop 2
	v_exp_f32_e32 v226, v210
	v_exp_f32_e32 v227, v211
	v_mfma_f32_16x16x32_f16 v[214:217], v[34:37], v[158:161], v[214:217]
	v_min_f32_e32 v228, s42, v212
	v_exp_f32_e32 v229, v213
	v_mfma_f32_16x16x32_f16 v[214:217], v[38:41], v[162:165], v[214:217]
	v_exp_f32_e32 v228, v228
	v_add_f32_e32 v227, 1.0, v227
	v_mfma_f32_16x16x32_f16 v[214:217], v[42:45], v[166:169], v[214:217]
	v_fma_f32 v230, v228, s41, s41
	v_rcp_f32_e32 v227, v227
	v_mfma_f32_16x16x32_f16 v[214:217], v[46:49], v[170:173], v[214:217]
	v_fma_f32 v230, v226, v230, v230
	v_rcp_f32_e32 v230, v230
	v_mfma_f32_16x16x32_f16 v[218:221], v[18:21], v[158:161], v[218:221]
	v_fma_f32 v226, -v228, v230, v230
	v_fma_f32 v200, v200, v227, v226
	v_mfma_f32_16x16x32_f16 v[218:221], v[14:17], v[162:165], v[218:221]
	v_exp_f32_e32 v226, v200
	s_nop 0
	v_add_f32_e32 v227, 1.0, v226
	v_mfma_f32_16x16x32_f16 v[218:221], v[10:13], v[166:169], v[218:221]
	v_fma_f32 v227, v229, v227, v227
	v_rcp_f32_e32 v227, v227
	v_mfma_f32_16x16x32_f16 v[218:221], v[26:29], v[170:173], v[218:221]
	v_fma_f32 v226, -v226, v227, v227
	v_exp_f32_e32 v231, v214
	v_mfma_f32_16x16x32_f16 v[222:225], v[2:5], v[158:161], v[222:225]
	v_exp_f32_e32 v232, v215
	v_min_f32_e32 v233, s42, v216
	v_mfma_f32_16x16x32_f16 v[222:225], v[6:9], v[162:165], v[222:225]
	v_exp_f32_e32 v234, v217
	v_exp_f32_e32 v233, v233
	v_mfma_f32_16x16x32_f16 v[222:225], v[22:25], v[166:169], v[222:225]
	v_exp_f32_e32 v236, v218
	v_add_f32_e32 v232, 1.0, v232
	v_mfma_f32_16x16x32_f16 v[222:225], v[30:33], v[170:173], v[222:225]
	v_fma_f32 v235, v233, s41, s41
	v_exp_f32_e32 v227, v219
	v_rcp_f32_e32 v232, v232
	v_fma_f32 v235, v231, v235, v235
	v_min_f32_e32 v228, s42, v220
	v_rcp_f32_e32 v235, v235
	v_exp_f32_e32 v229, v221
	v_fma_f32 v231, -v233, v235, v235
	v_fma_f32 v201, v201, v232, v231
	v_exp_f32_e32 v231, v201
	v_exp_f32_e32 v228, v228
	v_add_f32_e32 v232, 1.0, v231
	v_fma_f32 v232, v234, v232, v232
	v_add_f32_e32 v227, 1.0, v227
	v_rcp_f32_e32 v232, v232
	v_mfma_f32_16x16x32_f16 v[146:149], v[114:117], v[158:161], v[146:149]
	v_fma_f32 v231, -v231, v232, v232
	v_fma_f32 v230, v228, s41, s41
	v_cvt_pk_f16_f32 v246, v226, v231
	v_mfma_f32_16x16x32_f16 v[146:149], v[118:121], v[162:165], v[146:149]
	v_exp_f32_e32 v231, v222
	v_rcp_f32_e32 v227, v227
	v_exp_f32_e32 v232, v223
	buffer_load_dwordx4 v[114:117], v189, s[80:83], s46 offen
	buffer_load_dwordx4 v[118:121], v208, s[80:83], s46 offen
	v_min_f32_e32 v233, s42, v224
	v_fma_f32 v230, v236, v230, v230
	v_exp_f32_e32 v234, v225
	s_waitcnt lgkmcnt(0)
	v_mfma_f32_16x16x32_f16 v[210:213], v[70:73], v[150:153], v[98:101]
	v_exp_f32_e32 v233, v233
	v_rcp_f32_e32 v230, v230
	v_add_f32_e32 v232, 1.0, v232
	v_mfma_f32_16x16x32_f16 v[214:217], v[74:77], v[150:153], v[102:105]
	v_fma_f32 v235, v233, s41, s41
	v_fma_f32 v236, -v228, v230, v230
	v_rcp_f32_e32 v232, v232
	v_fma_f32 v235, v231, v235, v235
	v_fma_f32 v198, v198, v227, v236
	v_rcp_f32_e32 v235, v235
	v_exp_f32_e32 v236, v198
	v_fma_f32 v231, -v233, v235, v235
	v_fma_f32 v199, v199, v232, v231
	v_exp_f32_e32 v231, v199
	v_add_f32_e32 v227, 1.0, v236
	v_add_f32_e32 v232, 1.0, v231
	v_fma_f32 v232, v234, v232, v232
	v_fma_f32 v227, v229, v227, v227
	v_rcp_f32_e32 v232, v232
	v_rcp_f32_e32 v227, v227
	v_fma_f32 v231, -v231, v232, v232
	v_fma_f32 v236, -v236, v227, v227
	v_cvt_pk_f16_f32 v247, v236, v231
	ds_write_b64 v250, v[246:247] offset:16384
	v_mfma_f32_16x16x32_f16 v[210:213], v[66:69], v[154:157], v[210:213]
	v_mfma_f32_16x16x32_f16 v[214:217], v[78:81], v[154:157], v[214:217]
	buffer_load_dwordx2 v[190:191], v209, s[60:63], s45 offen
	s_add_i32 s45, s45, 0x400000
	s_add_i32 s46, s46, 0x10000
	s_waitcnt lgkmcnt(0)
	s_barrier
	ds_read_b128 v[158:161], v248 offset:8192
	ds_read_b128 v[162:165], v248 offset:9216
	ds_read_b128 v[166:169], v249 offset:10240
	ds_read_b128 v[170:173], v249 offset:11264
	v_mfma_f32_16x16x32_f16 v[218:221], v[82:85], v[150:153], v[106:109]
	v_mfma_f32_16x16x32_f16 v[222:225], v[90:93], v[150:153], v[110:113]
	v_mfma_f32_16x16x32_f16 v[218:221], v[86:89], v[154:157], v[218:221]
	v_mfma_f32_16x16x32_f16 v[222:225], v[94:97], v[154:157], v[222:225]
	s_waitcnt lgkmcnt(2)
	v_mfma_f32_16x16x32_f16 v[210:213], v[54:57], v[158:161], v[210:213]
	v_mfma_f32_16x16x32_f16 v[210:213], v[58:61], v[162:165], v[210:213]
	s_waitcnt lgkmcnt(0)
	v_mfma_f32_16x16x32_f16 v[210:213], v[62:65], v[166:169], v[210:213]
	v_mfma_f32_16x16x32_f16 v[210:213], v[50:53], v[170:173], v[210:213]
	s_waitcnt vmcnt(9)
	v_cvt_pk_f16_f32 v251, v196, v197
	ds_write_b32 v1, v251 offset:4096
	ds_read_b128 v[150:153], v186 offset:2048
	ds_read_b128 v[154:157], v186 offset:3072
	s_nop 2
	v_exp_f32_e32 v226, v210
	v_exp_f32_e32 v227, v211
	v_mfma_f32_16x16x32_f16 v[214:217], v[34:37], v[158:161], v[214:217]
	v_min_f32_e32 v228, s42, v212
	v_exp_f32_e32 v229, v213
	v_mfma_f32_16x16x32_f16 v[214:217], v[38:41], v[162:165], v[214:217]
	v_exp_f32_e32 v228, v228
	v_add_f32_e32 v227, 1.0, v227
	v_mfma_f32_16x16x32_f16 v[214:217], v[42:45], v[166:169], v[214:217]
	v_fma_f32 v230, v228, s41, s41
	v_rcp_f32_e32 v227, v227
	v_mfma_f32_16x16x32_f16 v[214:217], v[46:49], v[170:173], v[214:217]
	v_fma_f32 v230, v226, v230, v230
	v_rcp_f32_e32 v230, v230
	v_mfma_f32_16x16x32_f16 v[218:221], v[18:21], v[158:161], v[218:221]
	v_fma_f32 v226, -v228, v230, v230
	v_fma_f32 v200, v200, v227, v226
	v_mfma_f32_16x16x32_f16 v[218:221], v[14:17], v[162:165], v[218:221]
	v_exp_f32_e32 v226, v200
	s_nop 0
	v_add_f32_e32 v227, 1.0, v226
	v_mfma_f32_16x16x32_f16 v[218:221], v[10:13], v[166:169], v[218:221]
	v_fma_f32 v227, v229, v227, v227
	v_rcp_f32_e32 v227, v227
	v_mfma_f32_16x16x32_f16 v[218:221], v[26:29], v[170:173], v[218:221]
	v_fma_f32 v226, -v226, v227, v227
	v_exp_f32_e32 v231, v214
	v_mfma_f32_16x16x32_f16 v[222:225], v[2:5], v[158:161], v[222:225]
	v_exp_f32_e32 v232, v215
	v_min_f32_e32 v233, s42, v216
	v_mfma_f32_16x16x32_f16 v[222:225], v[6:9], v[162:165], v[222:225]
	v_exp_f32_e32 v234, v217
	v_exp_f32_e32 v233, v233
	v_mfma_f32_16x16x32_f16 v[222:225], v[22:25], v[166:169], v[222:225]
	v_exp_f32_e32 v236, v218
	v_add_f32_e32 v232, 1.0, v232
	v_mfma_f32_16x16x32_f16 v[222:225], v[30:33], v[170:173], v[222:225]
	v_fma_f32 v235, v233, s41, s41
	v_exp_f32_e32 v227, v219
	v_rcp_f32_e32 v232, v232
	v_fma_f32 v235, v231, v235, v235
	v_min_f32_e32 v228, s42, v220
	v_rcp_f32_e32 v235, v235
	v_exp_f32_e32 v229, v221
	v_fma_f32 v231, -v233, v235, v235
	v_fma_f32 v201, v201, v232, v231
	v_exp_f32_e32 v231, v201
	v_exp_f32_e32 v228, v228
	v_add_f32_e32 v232, 1.0, v231
	v_fma_f32 v232, v234, v232, v232
	v_add_f32_e32 v227, 1.0, v227
	v_rcp_f32_e32 v232, v232
	v_mfma_f32_16x16x32_f16 v[146:149], v[138:141], v[158:161], v[146:149]
	v_fma_f32 v231, -v231, v232, v232
	v_fma_f32 v230, v228, s41, s41
	v_cvt_pk_f16_f32 v246, v226, v231
	v_mfma_f32_16x16x32_f16 v[146:149], v[142:145], v[162:165], v[146:149]
	v_exp_f32_e32 v231, v222
	v_rcp_f32_e32 v227, v227
	v_exp_f32_e32 v232, v223
	buffer_load_dwordx4 v[138:141], v189, s[68:71], s46 offen
	buffer_load_dwordx4 v[142:145], v208, s[68:71], s46 offen
	v_min_f32_e32 v233, s42, v224
	v_fma_f32 v230, v236, v230, v230
	v_exp_f32_e32 v234, v225
	s_waitcnt lgkmcnt(0)
	v_mfma_f32_16x16x32_f16 v[210:213], v[70:73], v[150:153], v[98:101]
	v_exp_f32_e32 v233, v233
	v_rcp_f32_e32 v230, v230
	v_add_f32_e32 v232, 1.0, v232
	v_mfma_f32_16x16x32_f16 v[214:217], v[74:77], v[150:153], v[102:105]
	v_fma_f32 v235, v233, s41, s41
	v_fma_f32 v236, -v228, v230, v230
	v_rcp_f32_e32 v232, v232
	v_fma_f32 v235, v231, v235, v235
	v_fma_f32 v198, v198, v227, v236
	v_rcp_f32_e32 v235, v235
	v_exp_f32_e32 v236, v198
	v_fma_f32 v231, -v233, v235, v235
	v_fma_f32 v199, v199, v232, v231
	v_exp_f32_e32 v231, v199
	v_add_f32_e32 v227, 1.0, v236
	v_add_f32_e32 v232, 1.0, v231
	v_fma_f32 v232, v234, v232, v232
	v_fma_f32 v227, v229, v227, v227
	v_rcp_f32_e32 v232, v232
	v_rcp_f32_e32 v227, v227
	v_fma_f32 v231, -v231, v232, v232
	v_fma_f32 v236, -v236, v227, v227
	v_cvt_pk_f16_f32 v247, v236, v231
	ds_write_b64 v250, v[246:247] offset:20480
	v_mfma_f32_16x16x32_f16 v[210:213], v[66:69], v[154:157], v[210:213]
	v_mfma_f32_16x16x32_f16 v[214:217], v[78:81], v[154:157], v[214:217]
	buffer_load_dwordx2 v[196:197], v209, s[48:51], s45 offen
	s_waitcnt lgkmcnt(0)
	s_barrier
	ds_read_b128 v[158:161], v248 offset:12288
	ds_read_b128 v[162:165], v248 offset:13312
	ds_read_b128 v[166:169], v249 offset:14336
	ds_read_b128 v[170:173], v249 offset:15360
	v_mfma_f32_16x16x32_f16 v[218:221], v[82:85], v[150:153], v[106:109]
	v_mfma_f32_16x16x32_f16 v[222:225], v[90:93], v[150:153], v[110:113]
	v_mfma_f32_16x16x32_f16 v[218:221], v[86:89], v[154:157], v[218:221]
	v_mfma_f32_16x16x32_f16 v[222:225], v[94:97], v[154:157], v[222:225]
	s_waitcnt lgkmcnt(2)
	v_mfma_f32_16x16x32_f16 v[210:213], v[54:57], v[158:161], v[210:213]
	v_mfma_f32_16x16x32_f16 v[210:213], v[58:61], v[162:165], v[210:213]
	s_waitcnt lgkmcnt(0)
	v_mfma_f32_16x16x32_f16 v[210:213], v[62:65], v[166:169], v[210:213]
	v_mfma_f32_16x16x32_f16 v[210:213], v[50:53], v[170:173], v[210:213]
	s_waitcnt vmcnt(9)
	v_cvt_pk_f16_f32 v251, v194, v195
	ds_write_b32 v1, v251 offset:6144
	ds_read_b128 v[150:153], v186 offset:4096
	ds_read_b128 v[154:157], v186 offset:5120
	s_nop 2
	v_exp_f32_e32 v226, v210
	v_exp_f32_e32 v227, v211
	v_mfma_f32_16x16x32_f16 v[214:217], v[34:37], v[158:161], v[214:217]
	v_min_f32_e32 v228, s42, v212
	v_exp_f32_e32 v229, v213
	v_mfma_f32_16x16x32_f16 v[214:217], v[38:41], v[162:165], v[214:217]
	v_exp_f32_e32 v228, v228
	v_add_f32_e32 v227, 1.0, v227
	v_mfma_f32_16x16x32_f16 v[214:217], v[42:45], v[166:169], v[214:217]
	v_fma_f32 v230, v228, s41, s41
	v_rcp_f32_e32 v227, v227
	v_mfma_f32_16x16x32_f16 v[214:217], v[46:49], v[170:173], v[214:217]
	v_fma_f32 v230, v226, v230, v230
	v_rcp_f32_e32 v230, v230
	v_mfma_f32_16x16x32_f16 v[218:221], v[18:21], v[158:161], v[218:221]
	v_fma_f32 v226, -v228, v230, v230
	v_fma_f32 v200, v200, v227, v226
	v_mfma_f32_16x16x32_f16 v[218:221], v[14:17], v[162:165], v[218:221]
	v_exp_f32_e32 v226, v200
	s_nop 0
	v_add_f32_e32 v227, 1.0, v226
	v_mfma_f32_16x16x32_f16 v[218:221], v[10:13], v[166:169], v[218:221]
	v_fma_f32 v227, v229, v227, v227
	v_rcp_f32_e32 v227, v227
	v_mfma_f32_16x16x32_f16 v[218:221], v[26:29], v[170:173], v[218:221]
	v_fma_f32 v226, -v226, v227, v227
	v_exp_f32_e32 v231, v214
	v_mfma_f32_16x16x32_f16 v[222:225], v[2:5], v[158:161], v[222:225]
	v_exp_f32_e32 v232, v215
	v_min_f32_e32 v233, s42, v216
	v_mfma_f32_16x16x32_f16 v[222:225], v[6:9], v[162:165], v[222:225]
	v_exp_f32_e32 v234, v217
	v_exp_f32_e32 v233, v233
	v_mfma_f32_16x16x32_f16 v[222:225], v[22:25], v[166:169], v[222:225]
	v_exp_f32_e32 v236, v218
	v_add_f32_e32 v232, 1.0, v232
	v_mfma_f32_16x16x32_f16 v[222:225], v[30:33], v[170:173], v[222:225]
	v_fma_f32 v235, v233, s41, s41
	v_exp_f32_e32 v227, v219
	v_rcp_f32_e32 v232, v232
	v_fma_f32 v235, v231, v235, v235
	v_min_f32_e32 v228, s42, v220
	v_rcp_f32_e32 v235, v235
	v_exp_f32_e32 v229, v221
	v_fma_f32 v231, -v233, v235, v235
	v_fma_f32 v201, v201, v232, v231
	v_exp_f32_e32 v231, v201
	v_exp_f32_e32 v228, v228
	v_add_f32_e32 v232, 1.0, v231
	v_fma_f32 v232, v234, v232, v232
	v_add_f32_e32 v227, 1.0, v227
	v_rcp_f32_e32 v232, v232
	v_mfma_f32_16x16x32_f16 v[146:149], v[130:133], v[158:161], v[146:149]
	v_fma_f32 v231, -v231, v232, v232
	v_fma_f32 v230, v228, s41, s41
	v_cvt_pk_f16_f32 v246, v226, v231
	v_mfma_f32_16x16x32_f16 v[146:149], v[134:137], v[162:165], v[146:149]
	v_exp_f32_e32 v231, v222
	v_rcp_f32_e32 v227, v227
	v_exp_f32_e32 v232, v223
	buffer_load_dwordx4 v[130:133], v189, s[72:75], s46 offen
	buffer_load_dwordx4 v[134:137], v208, s[72:75], s46 offen
	v_min_f32_e32 v233, s42, v224
	v_fma_f32 v230, v236, v230, v230
	v_exp_f32_e32 v234, v225
	s_waitcnt lgkmcnt(0)
	v_mfma_f32_16x16x32_f16 v[210:213], v[70:73], v[150:153], v[98:101]
	v_exp_f32_e32 v233, v233
	v_rcp_f32_e32 v230, v230
	v_add_f32_e32 v232, 1.0, v232
	v_mfma_f32_16x16x32_f16 v[214:217], v[74:77], v[150:153], v[102:105]
	v_fma_f32 v235, v233, s41, s41
	v_fma_f32 v236, -v228, v230, v230
	v_rcp_f32_e32 v232, v232
	v_fma_f32 v235, v231, v235, v235
	v_fma_f32 v198, v198, v227, v236
	v_rcp_f32_e32 v235, v235
	v_exp_f32_e32 v236, v198
	v_fma_f32 v231, -v233, v235, v235
	v_fma_f32 v199, v199, v232, v231
	v_exp_f32_e32 v231, v199
	v_add_f32_e32 v227, 1.0, v236
	v_add_f32_e32 v232, 1.0, v231
	v_fma_f32 v232, v234, v232, v232
	v_fma_f32 v227, v229, v227, v227
	v_rcp_f32_e32 v232, v232
	v_rcp_f32_e32 v227, v227
	v_fma_f32 v231, -v231, v232, v232
	v_fma_f32 v236, -v236, v227, v227
	v_cvt_pk_f16_f32 v247, v236, v231
	ds_write_b64 v250, v[246:247] offset:24576
	v_mfma_f32_16x16x32_f16 v[210:213], v[66:69], v[154:157], v[210:213]
	v_mfma_f32_16x16x32_f16 v[214:217], v[78:81], v[154:157], v[214:217]
	buffer_load_dwordx2 v[194:195], v209, s[52:55], s45 offen
	v_add_u32_e32 v250, 0x4000, v250
	v_add_u32_e32 v248, 0x4000, v248
	v_add_u32_e32 v249, 0x4000, v249
	s_waitcnt lgkmcnt(0)
	s_barrier
	s_cmp_lt_u32 s46, 0xa0000
	s_cbranch_scc1 .Lmy_loopb
	ds_read_b128 v[158:161], v248 offset:0
	ds_read_b128 v[162:165], v248 offset:1024
	ds_read_b128 v[166:169], v249 offset:2048
	ds_read_b128 v[170:173], v249 offset:3072
	v_mfma_f32_16x16x32_f16 v[218:221], v[82:85], v[150:153], v[106:109]
	v_mfma_f32_16x16x32_f16 v[222:225], v[90:93], v[150:153], v[110:113]
	v_mfma_f32_16x16x32_f16 v[218:221], v[86:89], v[154:157], v[218:221]
	v_mfma_f32_16x16x32_f16 v[222:225], v[94:97], v[154:157], v[222:225]
	s_waitcnt lgkmcnt(2)
	v_mfma_f32_16x16x32_f16 v[210:213], v[54:57], v[158:161], v[210:213]
	v_mfma_f32_16x16x32_f16 v[210:213], v[58:61], v[162:165], v[210:213]
	s_waitcnt lgkmcnt(0)
	v_mfma_f32_16x16x32_f16 v[210:213], v[62:65], v[166:169], v[210:213]
	v_mfma_f32_16x16x32_f16 v[210:213], v[50:53], v[170:173], v[210:213]
	s_waitcnt vmcnt(9)
	v_cvt_pk_f16_f32 v251, v192, v193
	ds_write_b32 v1, v251 offset:0
	ds_read_b128 v[150:153], v186 offset:6144
	ds_read_b128 v[154:157], v186 offset:7168
	s_nop 2
	v_exp_f32_e32 v226, v210
	v_exp_f32_e32 v227, v211
	v_mfma_f32_16x16x32_f16 v[214:217], v[34:37], v[158:161], v[214:217]
	v_min_f32_e32 v228, s42, v212
	v_exp_f32_e32 v229, v213
	v_mfma_f32_16x16x32_f16 v[214:217], v[38:41], v[162:165], v[214:217]
	v_exp_f32_e32 v228, v228
	v_add_f32_e32 v227, 1.0, v227
	v_mfma_f32_16x16x32_f16 v[214:217], v[42:45], v[166:169], v[214:217]
	v_fma_f32 v230, v228, s41, s41
	v_rcp_f32_e32 v227, v227
	v_mfma_f32_16x16x32_f16 v[214:217], v[46:49], v[170:173], v[214:217]
	v_fma_f32 v230, v226, v230, v230
	v_rcp_f32_e32 v230, v230
	v_mfma_f32_16x16x32_f16 v[218:221], v[18:21], v[158:161], v[218:221]
	v_fma_f32 v226, -v228, v230, v230
	v_fma_f32 v200, v200, v227, v226
	v_mfma_f32_16x16x32_f16 v[218:221], v[14:17], v[162:165], v[218:221]
	v_min_f32_e32 v226, s42, v200
	v_exp_f32_e32 v226, v226
	v_mfma_f32_16x16x32_f16 v[218:221], v[10:13], v[166:169], v[218:221]
	v_add_f32_e32 v227, 1.0, v226
	v_fma_f32 v227, v229, v227, v227
	v_mfma_f32_16x16x32_f16 v[218:221], v[26:29], v[170:173], v[218:221]
	v_rcp_f32_e32 v227, v227
	v_exp_f32_e32 v231, v214
	v_mfma_f32_16x16x32_f16 v[222:225], v[2:5], v[158:161], v[222:225]
	v_exp_f32_e32 v232, v215
	v_fma_f32 v226, -v226, v227, v227
	v_mfma_f32_16x16x32_f16 v[222:225], v[6:9], v[162:165], v[222:225]
	v_min_f32_e32 v233, s42, v216
	v_exp_f32_e32 v234, v217
	v_mfma_f32_16x16x32_f16 v[222:225], v[22:25], v[166:169], v[222:225]
	v_exp_f32_e32 v236, v218
	v_exp_f32_e32 v233, v233
	v_mfma_f32_16x16x32_f16 v[222:225], v[30:33], v[170:173], v[222:225]
	v_add_f32_e32 v232, 1.0, v232
	v_exp_f32_e32 v227, v219
	v_fma_f32 v235, v233, s41, s41
	v_rcp_f32_e32 v232, v232
	v_min_f32_e32 v228, s42, v220
	v_fma_f32 v235, v231, v235, v235
	v_rcp_f32_e32 v235, v235
	v_exp_f32_e32 v229, v221
	v_fma_f32 v231, -v233, v235, v235
	v_fma_f32 v201, v201, v232, v231
	v_exp_f32_e32 v228, v228
	v_min_f32_e32 v231, s42, v201
	v_exp_f32_e32 v231, v231
	v_add_f32_e32 v227, 1.0, v227
	v_add_f32_e32 v232, 1.0, v231
	v_mfma_f32_16x16x32_f16 v[146:149], v[122:125], v[158:161], v[146:149]
	v_fma_f32 v232, v234, v232, v232
	v_fma_f32 v230, v228, s41, s41
	v_rcp_f32_e32 v232, v232
	v_mfma_f32_16x16x32_f16 v[146:149], v[126:129], v[162:165], v[146:149]
	v_fma_f32 v231, -v231, v232, v232
	v_rcp_f32_e32 v227, v227
	v_cvt_pk_f16_f32 v246, v226, v231
	buffer_load_dwordx4 v[122:125], v189, s[76:79], s46 offen
	buffer_load_dwordx4 v[126:129], v208, s[76:79], s46 offen
	v_exp_f32_e32 v231, v222
	v_fma_f32 v230, v236, v230, v230
	v_exp_f32_e32 v232, v223
	s_waitcnt lgkmcnt(0)
	v_mfma_f32_16x16x32_f16 v[210:213], v[70:73], v[150:153], v[98:101]
	v_min_f32_e32 v233, s42, v224
	v_rcp_f32_e32 v230, v230
	v_exp_f32_e32 v234, v225
	v_mfma_f32_16x16x32_f16 v[214:217], v[74:77], v[150:153], v[102:105]
	v_exp_f32_e32 v233, v233
	v_fma_f32 v236, -v228, v230, v230
	v_add_f32_e32 v232, 1.0, v232
	v_fma_f32 v235, v233, s41, s41
	v_fma_f32 v198, v198, v227, v236
	v_rcp_f32_e32 v232, v232
	v_fma_f32 v235, v231, v235, v235
	v_min_f32_e32 v236, s42, v198
	v_rcp_f32_e32 v235, v235
	v_exp_f32_e32 v236, v236
	v_fma_f32 v231, -v233, v235, v235
	v_fma_f32 v199, v199, v232, v231
	v_min_f32_e32 v231, s42, v199
	v_add_f32_e32 v227, 1.0, v236
	v_exp_f32_e32 v231, v231
	v_fma_f32 v227, v229, v227, v227
	v_add_f32_e32 v232, 1.0, v231
	v_rcp_f32_e32 v227, v227
	v_fma_f32 v232, v234, v232, v232
	v_fma_f32 v236, -v236, v227, v227
	v_rcp_f32_e32 v232, v232
	s_nop 0
	v_fma_f32 v231, -v231, v232, v232
	v_cvt_pk_f16_f32 v247, v236, v231
	ds_write_b64 v250, v[246:247] offset:12288
	v_mfma_f32_16x16x32_f16 v[210:213], v[66:69], v[154:157], v[210:213]
	v_mfma_f32_16x16x32_f16 v[214:217], v[78:81], v[154:157], v[214:217]
	buffer_load_dwordx2 v[192:193], v209, s[56:59], s45 offen
	s_waitcnt lgkmcnt(0)
	s_barrier
	ds_read_b128 v[158:161], v248 offset:4096
	ds_read_b128 v[162:165], v248 offset:5120
	ds_read_b128 v[166:169], v249 offset:6144
	ds_read_b128 v[170:173], v249 offset:7168
	v_mfma_f32_16x16x32_f16 v[218:221], v[82:85], v[150:153], v[106:109]
	v_mfma_f32_16x16x32_f16 v[222:225], v[90:93], v[150:153], v[110:113]
	v_mfma_f32_16x16x32_f16 v[218:221], v[86:89], v[154:157], v[218:221]
	v_mfma_f32_16x16x32_f16 v[222:225], v[94:97], v[154:157], v[222:225]
	s_waitcnt lgkmcnt(2)
	v_mfma_f32_16x16x32_f16 v[210:213], v[54:57], v[158:161], v[210:213]
	v_mfma_f32_16x16x32_f16 v[210:213], v[58:61], v[162:165], v[210:213]
	s_waitcnt lgkmcnt(0)
	v_mfma_f32_16x16x32_f16 v[210:213], v[62:65], v[166:169], v[210:213]
	v_mfma_f32_16x16x32_f16 v[210:213], v[50:53], v[170:173], v[210:213]
	s_waitcnt vmcnt(9)
	v_cvt_pk_f16_f32 v251, v190, v191
	ds_write_b32 v1, v251 offset:2048
	ds_read_b128 v[150:153], v186 offset:0
	ds_read_b128 v[154:157], v186 offset:1024
	s_nop 2
	v_exp_f32_e32 v226, v210
	v_exp_f32_e32 v227, v211
	v_mfma_f32_16x16x32_f16 v[214:217], v[34:37], v[158:161], v[214:217]
	v_min_f32_e32 v228, s42, v212
	v_exp_f32_e32 v229, v213
	v_mfma_f32_16x16x32_f16 v[214:217], v[38:41], v[162:165], v[214:217]
	v_exp_f32_e32 v228, v228
	v_add_f32_e32 v227, 1.0, v227
	v_mfma_f32_16x16x32_f16 v[214:217], v[42:45], v[166:169], v[214:217]
	v_fma_f32 v230, v228, s41, s41
	v_rcp_f32_e32 v227, v227
	v_mfma_f32_16x16x32_f16 v[214:217], v[46:49], v[170:173], v[214:217]
	v_fma_f32 v230, v226, v230, v230
	v_rcp_f32_e32 v230, v230
	v_mfma_f32_16x16x32_f16 v[218:221], v[18:21], v[158:161], v[218:221]
	v_fma_f32 v226, -v228, v230, v230
	v_fma_f32 v200, v200, v227, v226
	v_mfma_f32_16x16x32_f16 v[218:221], v[14:17], v[162:165], v[218:221]
	v_min_f32_e32 v226, s42, v200
	v_exp_f32_e32 v226, v226
	v_mfma_f32_16x16x32_f16 v[218:221], v[10:13], v[166:169], v[218:221]
	v_add_f32_e32 v227, 1.0, v226
	v_fma_f32 v227, v229, v227, v227
	v_mfma_f32_16x16x32_f16 v[218:221], v[26:29], v[170:173], v[218:221]
	v_rcp_f32_e32 v227, v227
	v_exp_f32_e32 v231, v214
	v_mfma_f32_16x16x32_f16 v[222:225], v[2:5], v[158:161], v[222:225]
	v_exp_f32_e32 v232, v215
	v_fma_f32 v226, -v226, v227, v227
	v_mfma_f32_16x16x32_f16 v[222:225], v[6:9], v[162:165], v[222:225]
	v_min_f32_e32 v233, s42, v216
	v_exp_f32_e32 v234, v217
	v_mfma_f32_16x16x32_f16 v[222:225], v[22:25], v[166:169], v[222:225]
	v_exp_f32_e32 v236, v218
	v_exp_f32_e32 v233, v233
	v_mfma_f32_16x16x32_f16 v[222:225], v[30:33], v[170:173], v[222:225]
	v_add_f32_e32 v232, 1.0, v232
	v_exp_f32_e32 v227, v219
	v_fma_f32 v235, v233, s41, s41
	v_rcp_f32_e32 v232, v232
	v_min_f32_e32 v228, s42, v220
	v_fma_f32 v235, v231, v235, v235
	v_rcp_f32_e32 v235, v235
	v_exp_f32_e32 v229, v221
	v_fma_f32 v231, -v233, v235, v235
	v_fma_f32 v201, v201, v232, v231
	v_exp_f32_e32 v228, v228
	v_min_f32_e32 v231, s42, v201
	v_exp_f32_e32 v231, v231
	v_add_f32_e32 v227, 1.0, v227
	v_add_f32_e32 v232, 1.0, v231
	v_mfma_f32_16x16x32_f16 v[146:149], v[114:117], v[158:161], v[146:149]
	v_fma_f32 v232, v234, v232, v232
	v_fma_f32 v230, v228, s41, s41
	v_rcp_f32_e32 v232, v232
	v_mfma_f32_16x16x32_f16 v[146:149], v[118:121], v[162:165], v[146:149]
	v_fma_f32 v231, -v231, v232, v232
	v_rcp_f32_e32 v227, v227
	v_cvt_pk_f16_f32 v246, v226, v231
	buffer_load_dwordx4 v[114:117], v189, s[80:83], s46 offen
	buffer_load_dwordx4 v[118:121], v208, s[80:83], s46 offen
	v_exp_f32_e32 v231, v222
	v_fma_f32 v230, v236, v230, v230
	v_exp_f32_e32 v232, v223
	s_waitcnt lgkmcnt(0)
	v_mfma_f32_16x16x32_f16 v[210:213], v[70:73], v[150:153], v[98:101]
	v_min_f32_e32 v233, s42, v224
	v_rcp_f32_e32 v230, v230
	v_exp_f32_e32 v234, v225
	v_mfma_f32_16x16x32_f16 v[214:217], v[74:77], v[150:153], v[102:105]
	v_exp_f32_e32 v233, v233
	v_fma_f32 v236, -v228, v230, v230
	v_add_f32_e32 v232, 1.0, v232
	v_fma_f32 v235, v233, s41, s41
	v_fma_f32 v198, v198, v227, v236
	v_rcp_f32_e32 v232, v232
	v_fma_f32 v235, v231, v235, v235
	v_min_f32_e32 v236, s42, v198
	v_rcp_f32_e32 v235, v235
	v_exp_f32_e32 v236, v236
	v_fma_f32 v231, -v233, v235, v235
	v_fma_f32 v199, v199, v232, v231
	v_min_f32_e32 v231, s42, v199
	v_add_f32_e32 v227, 1.0, v236
	v_exp_f32_e32 v231, v231
	v_fma_f32 v227, v229, v227, v227
	v_add_f32_e32 v232, 1.0, v231
	v_rcp_f32_e32 v227, v227
	v_fma_f32 v232, v234, v232, v232
	v_fma_f32 v236, -v236, v227, v227
	v_rcp_f32_e32 v232, v232
	s_nop 0
	v_fma_f32 v231, -v231, v232, v232
	v_cvt_pk_f16_f32 v247, v236, v231
	ds_write_b64 v250, v[246:247] offset:16384
	v_mfma_f32_16x16x32_f16 v[210:213], v[66:69], v[154:157], v[210:213]
	v_mfma_f32_16x16x32_f16 v[214:217], v[78:81], v[154:157], v[214:217]
	buffer_load_dwordx2 v[190:191], v209, s[60:63], s45 offen
	s_add_i32 s45, s45, 0x400000
	s_add_i32 s46, s46, 0x10000
	s_waitcnt lgkmcnt(0)
	s_barrier
	ds_read_b128 v[158:161], v248 offset:8192
	ds_read_b128 v[162:165], v248 offset:9216
	ds_read_b128 v[166:169], v249 offset:10240
	ds_read_b128 v[170:173], v249 offset:11264
	v_mfma_f32_16x16x32_f16 v[218:221], v[82:85], v[150:153], v[106:109]
	v_mfma_f32_16x16x32_f16 v[222:225], v[90:93], v[150:153], v[110:113]
	v_mfma_f32_16x16x32_f16 v[218:221], v[86:89], v[154:157], v[218:221]
	v_mfma_f32_16x16x32_f16 v[222:225], v[94:97], v[154:157], v[222:225]
	s_waitcnt lgkmcnt(2)
	v_mfma_f32_16x16x32_f16 v[210:213], v[54:57], v[158:161], v[210:213]
	v_mfma_f32_16x16x32_f16 v[210:213], v[58:61], v[162:165], v[210:213]
	s_waitcnt lgkmcnt(0)
	v_mfma_f32_16x16x32_f16 v[210:213], v[62:65], v[166:169], v[210:213]
	v_mfma_f32_16x16x32_f16 v[210:213], v[50:53], v[170:173], v[210:213]
	s_waitcnt vmcnt(9)
	v_cvt_pk_f16_f32 v251, v196, v197
	ds_write_b32 v1, v251 offset:4096
	ds_read_b128 v[150:153], v186 offset:2048
	ds_read_b128 v[154:157], v186 offset:3072
	s_nop 2
	v_exp_f32_e32 v226, v210
	v_exp_f32_e32 v227, v211
	v_mfma_f32_16x16x32_f16 v[214:217], v[34:37], v[158:161], v[214:217]
	v_min_f32_e32 v228, s42, v212
	v_exp_f32_e32 v229, v213
	v_mfma_f32_16x16x32_f16 v[214:217], v[38:41], v[162:165], v[214:217]
	v_exp_f32_e32 v228, v228
	v_add_f32_e32 v227, 1.0, v227
	v_mfma_f32_16x16x32_f16 v[214:217], v[42:45], v[166:169], v[214:217]
	v_fma_f32 v230, v228, s41, s41
	v_rcp_f32_e32 v227, v227
	v_mfma_f32_16x16x32_f16 v[214:217], v[46:49], v[170:173], v[214:217]
	v_fma_f32 v230, v226, v230, v230
	v_rcp_f32_e32 v230, v230
	v_mfma_f32_16x16x32_f16 v[218:221], v[18:21], v[158:161], v[218:221]
	v_fma_f32 v226, -v228, v230, v230
	v_fma_f32 v200, v200, v227, v226
	v_mfma_f32_16x16x32_f16 v[218:221], v[14:17], v[162:165], v[218:221]
	v_min_f32_e32 v226, s42, v200
	v_exp_f32_e32 v226, v226
	v_mfma_f32_16x16x32_f16 v[218:221], v[10:13], v[166:169], v[218:221]
	v_add_f32_e32 v227, 1.0, v226
	v_fma_f32 v227, v229, v227, v227
	v_mfma_f32_16x16x32_f16 v[218:221], v[26:29], v[170:173], v[218:221]
	v_rcp_f32_e32 v227, v227
	v_exp_f32_e32 v231, v214
	v_mfma_f32_16x16x32_f16 v[222:225], v[2:5], v[158:161], v[222:225]
	v_exp_f32_e32 v232, v215
	v_fma_f32 v226, -v226, v227, v227
	v_mfma_f32_16x16x32_f16 v[222:225], v[6:9], v[162:165], v[222:225]
	v_min_f32_e32 v233, s42, v216
	v_exp_f32_e32 v234, v217
	v_mfma_f32_16x16x32_f16 v[222:225], v[22:25], v[166:169], v[222:225]
	v_exp_f32_e32 v236, v218
	v_exp_f32_e32 v233, v233
	v_mfma_f32_16x16x32_f16 v[222:225], v[30:33], v[170:173], v[222:225]
	v_add_f32_e32 v232, 1.0, v232
	v_exp_f32_e32 v227, v219
	v_fma_f32 v235, v233, s41, s41
	v_rcp_f32_e32 v232, v232
	v_min_f32_e32 v228, s42, v220
	v_fma_f32 v235, v231, v235, v235
	v_rcp_f32_e32 v235, v235
	v_exp_f32_e32 v229, v221
	v_fma_f32 v231, -v233, v235, v235
	v_fma_f32 v201, v201, v232, v231
	v_exp_f32_e32 v228, v228
	v_min_f32_e32 v231, s42, v201
	v_exp_f32_e32 v231, v231
	v_add_f32_e32 v227, 1.0, v227
	v_add_f32_e32 v232, 1.0, v231
	v_mfma_f32_16x16x32_f16 v[146:149], v[138:141], v[158:161], v[146:149]
	v_fma_f32 v232, v234, v232, v232
	v_fma_f32 v230, v228, s41, s41
	v_rcp_f32_e32 v232, v232
	v_mfma_f32_16x16x32_f16 v[146:149], v[142:145], v[162:165], v[146:149]
	v_fma_f32 v231, -v231, v232, v232
	v_rcp_f32_e32 v227, v227
	v_cvt_pk_f16_f32 v246, v226, v231
	buffer_load_dwordx4 v[138:141], v189, s[68:71], s46 offen
	buffer_load_dwordx4 v[142:145], v208, s[68:71], s46 offen
	v_exp_f32_e32 v231, v222
	v_fma_f32 v230, v236, v230, v230
	v_exp_f32_e32 v232, v223
	s_waitcnt lgkmcnt(0)
	v_mfma_f32_16x16x32_f16 v[210:213], v[70:73], v[150:153], v[98:101]
	v_min_f32_e32 v233, s42, v224
	v_rcp_f32_e32 v230, v230
	v_exp_f32_e32 v234, v225
	v_mfma_f32_16x16x32_f16 v[214:217], v[74:77], v[150:153], v[102:105]
	v_exp_f32_e32 v233, v233
	v_fma_f32 v236, -v228, v230, v230
	v_add_f32_e32 v232, 1.0, v232
	v_fma_f32 v235, v233, s41, s41
	v_fma_f32 v198, v198, v227, v236
	v_rcp_f32_e32 v232, v232
	v_fma_f32 v235, v231, v235, v235
	v_min_f32_e32 v236, s42, v198
	v_rcp_f32_e32 v235, v235
	v_exp_f32_e32 v236, v236
	v_fma_f32 v231, -v233, v235, v235
	v_fma_f32 v199, v199, v232, v231
	v_min_f32_e32 v231, s42, v199
	v_add_f32_e32 v227, 1.0, v236
	v_exp_f32_e32 v231, v231
	v_fma_f32 v227, v229, v227, v227
	v_add_f32_e32 v232, 1.0, v231
	v_rcp_f32_e32 v227, v227
	v_fma_f32 v232, v234, v232, v232
	v_fma_f32 v236, -v236, v227, v227
	v_rcp_f32_e32 v232, v232
	s_nop 0
	v_fma_f32 v231, -v231, v232, v232
	v_cvt_pk_f16_f32 v247, v236, v231
	ds_write_b64 v250, v[246:247] offset:20480
	v_mfma_f32_16x16x32_f16 v[210:213], v[66:69], v[154:157], v[210:213]
	v_mfma_f32_16x16x32_f16 v[214:217], v[78:81], v[154:157], v[214:217]
	buffer_load_dwordx2 v[196:197], v209, s[48:51], s45 offen
	s_waitcnt lgkmcnt(0)
	s_barrier
	ds_read_b128 v[158:161], v248 offset:12288
	ds_read_b128 v[162:165], v248 offset:13312
	ds_read_b128 v[166:169], v249 offset:14336
	ds_read_b128 v[170:173], v249 offset:15360
	v_mfma_f32_16x16x32_f16 v[218:221], v[82:85], v[150:153], v[106:109]
	v_mfma_f32_16x16x32_f16 v[222:225], v[90:93], v[150:153], v[110:113]
	v_mfma_f32_16x16x32_f16 v[218:221], v[86:89], v[154:157], v[218:221]
	v_mfma_f32_16x16x32_f16 v[222:225], v[94:97], v[154:157], v[222:225]
	s_waitcnt lgkmcnt(2)
	v_mfma_f32_16x16x32_f16 v[210:213], v[54:57], v[158:161], v[210:213]
	v_mfma_f32_16x16x32_f16 v[210:213], v[58:61], v[162:165], v[210:213]
	s_waitcnt lgkmcnt(0)
	v_mfma_f32_16x16x32_f16 v[210:213], v[62:65], v[166:169], v[210:213]
	v_mfma_f32_16x16x32_f16 v[210:213], v[50:53], v[170:173], v[210:213]
	s_waitcnt vmcnt(9)
	v_cvt_pk_f16_f32 v251, v194, v195
	ds_write_b32 v1, v251 offset:6144
	ds_read_b128 v[150:153], v186 offset:4096
	ds_read_b128 v[154:157], v186 offset:5120
	s_nop 2
	v_exp_f32_e32 v226, v210
	v_exp_f32_e32 v227, v211
	v_mfma_f32_16x16x32_f16 v[214:217], v[34:37], v[158:161], v[214:217]
	v_min_f32_e32 v228, s42, v212
	v_exp_f32_e32 v229, v213
	v_mfma_f32_16x16x32_f16 v[214:217], v[38:41], v[162:165], v[214:217]
	v_exp_f32_e32 v228, v228
	v_add_f32_e32 v227, 1.0, v227
	v_mfma_f32_16x16x32_f16 v[214:217], v[42:45], v[166:169], v[214:217]
	v_fma_f32 v230, v228, s41, s41
	v_rcp_f32_e32 v227, v227
	v_mfma_f32_16x16x32_f16 v[214:217], v[46:49], v[170:173], v[214:217]
	v_fma_f32 v230, v226, v230, v230
	v_rcp_f32_e32 v230, v230
	v_mfma_f32_16x16x32_f16 v[218:221], v[18:21], v[158:161], v[218:221]
	v_fma_f32 v226, -v228, v230, v230
	v_fma_f32 v200, v200, v227, v226
	v_mfma_f32_16x16x32_f16 v[218:221], v[14:17], v[162:165], v[218:221]
	v_min_f32_e32 v226, s42, v200
	v_exp_f32_e32 v226, v226
	v_mfma_f32_16x16x32_f16 v[218:221], v[10:13], v[166:169], v[218:221]
	v_add_f32_e32 v227, 1.0, v226
	v_fma_f32 v227, v229, v227, v227
	v_mfma_f32_16x16x32_f16 v[218:221], v[26:29], v[170:173], v[218:221]
	v_rcp_f32_e32 v227, v227
	v_exp_f32_e32 v231, v214
	v_mfma_f32_16x16x32_f16 v[222:225], v[2:5], v[158:161], v[222:225]
	v_exp_f32_e32 v232, v215
	v_fma_f32 v226, -v226, v227, v227
	v_mfma_f32_16x16x32_f16 v[222:225], v[6:9], v[162:165], v[222:225]
	v_min_f32_e32 v233, s42, v216
	v_exp_f32_e32 v234, v217
	v_mfma_f32_16x16x32_f16 v[222:225], v[22:25], v[166:169], v[222:225]
	v_exp_f32_e32 v236, v218
	v_exp_f32_e32 v233, v233
	v_mfma_f32_16x16x32_f16 v[222:225], v[30:33], v[170:173], v[222:225]
	v_add_f32_e32 v232, 1.0, v232
	v_exp_f32_e32 v227, v219
	v_fma_f32 v235, v233, s41, s41
	v_rcp_f32_e32 v232, v232
	v_min_f32_e32 v228, s42, v220
	v_fma_f32 v235, v231, v235, v235
	v_rcp_f32_e32 v235, v235
	v_exp_f32_e32 v229, v221
	v_fma_f32 v231, -v233, v235, v235
	v_fma_f32 v201, v201, v232, v231
	v_exp_f32_e32 v228, v228
	v_min_f32_e32 v231, s42, v201
	v_exp_f32_e32 v231, v231
	v_add_f32_e32 v227, 1.0, v227
	v_add_f32_e32 v232, 1.0, v231
	v_mfma_f32_16x16x32_f16 v[146:149], v[130:133], v[158:161], v[146:149]
	v_fma_f32 v232, v234, v232, v232
	v_fma_f32 v230, v228, s41, s41
	v_rcp_f32_e32 v232, v232
	v_mfma_f32_16x16x32_f16 v[146:149], v[134:137], v[162:165], v[146:149]
	v_fma_f32 v231, -v231, v232, v232
	v_rcp_f32_e32 v227, v227
	v_cvt_pk_f16_f32 v246, v226, v231
	buffer_load_dwordx4 v[130:133], v189, s[72:75], s46 offen
	buffer_load_dwordx4 v[134:137], v208, s[72:75], s46 offen
	v_exp_f32_e32 v231, v222
	v_fma_f32 v230, v236, v230, v230
	v_exp_f32_e32 v232, v223
	s_waitcnt lgkmcnt(0)
	v_mfma_f32_16x16x32_f16 v[210:213], v[70:73], v[150:153], v[98:101]
	v_min_f32_e32 v233, s42, v224
	v_rcp_f32_e32 v230, v230
	v_exp_f32_e32 v234, v225
	v_mfma_f32_16x16x32_f16 v[214:217], v[74:77], v[150:153], v[102:105]
	v_exp_f32_e32 v233, v233
	v_fma_f32 v236, -v228, v230, v230
	v_add_f32_e32 v232, 1.0, v232
	v_fma_f32 v235, v233, s41, s41
	v_fma_f32 v198, v198, v227, v236
	v_rcp_f32_e32 v232, v232
	v_fma_f32 v235, v231, v235, v235
	v_min_f32_e32 v236, s42, v198
	v_rcp_f32_e32 v235, v235
	v_exp_f32_e32 v236, v236
	v_fma_f32 v231, -v233, v235, v235
	v_fma_f32 v199, v199, v232, v231
	v_min_f32_e32 v231, s42, v199
	v_add_f32_e32 v227, 1.0, v236
	v_exp_f32_e32 v231, v231
	v_fma_f32 v227, v229, v227, v227
	v_add_f32_e32 v232, 1.0, v231
	v_rcp_f32_e32 v227, v227
	v_fma_f32 v232, v234, v232, v232
	v_fma_f32 v236, -v236, v227, v227
	v_rcp_f32_e32 v232, v232
	s_nop 0
	v_fma_f32 v231, -v231, v232, v232
	v_cvt_pk_f16_f32 v247, v236, v231
	ds_write_b64 v250, v[246:247] offset:24576
	v_mfma_f32_16x16x32_f16 v[210:213], v[66:69], v[154:157], v[210:213]
	v_mfma_f32_16x16x32_f16 v[214:217], v[78:81], v[154:157], v[214:217]
	buffer_load_dwordx2 v[194:195], v209, s[52:55], s45 offen
	v_add_u32_e32 v250, 0x4000, v250
	v_add_u32_e32 v248, 0x4000, v248
	v_add_u32_e32 v249, 0x4000, v249
	s_waitcnt lgkmcnt(0)
	s_barrier
	ds_read_b128 v[158:161], v248 offset:0
	ds_read_b128 v[162:165], v248 offset:1024
	ds_read_b128 v[166:169], v249 offset:2048
	ds_read_b128 v[170:173], v249 offset:3072
	v_mfma_f32_16x16x32_f16 v[218:221], v[82:85], v[150:153], v[106:109]
	v_mfma_f32_16x16x32_f16 v[222:225], v[90:93], v[150:153], v[110:113]
	v_mfma_f32_16x16x32_f16 v[218:221], v[86:89], v[154:157], v[218:221]
	v_mfma_f32_16x16x32_f16 v[222:225], v[94:97], v[154:157], v[222:225]
	s_waitcnt lgkmcnt(2)
	v_mfma_f32_16x16x32_f16 v[210:213], v[54:57], v[158:161], v[210:213]
	v_mfma_f32_16x16x32_f16 v[210:213], v[58:61], v[162:165], v[210:213]
	s_waitcnt lgkmcnt(0)
	v_mfma_f32_16x16x32_f16 v[210:213], v[62:65], v[166:169], v[210:213]
	v_mfma_f32_16x16x32_f16 v[210:213], v[50:53], v[170:173], v[210:213]
	s_waitcnt vmcnt(9)
	v_cvt_pk_f16_f32 v251, v192, v193
	ds_write_b32 v1, v251 offset:0
	ds_read_b128 v[150:153], v186 offset:6144
	ds_read_b128 v[154:157], v186 offset:7168
	s_nop 2
	v_exp_f32_e32 v226, v210
	v_exp_f32_e32 v227, v211
	v_mfma_f32_16x16x32_f16 v[214:217], v[34:37], v[158:161], v[214:217]
	v_min_f32_e32 v228, s42, v212
	v_exp_f32_e32 v229, v213
	v_mfma_f32_16x16x32_f16 v[214:217], v[38:41], v[162:165], v[214:217]
	v_exp_f32_e32 v228, v228
	v_add_f32_e32 v227, 1.0, v227
	v_mfma_f32_16x16x32_f16 v[214:217], v[42:45], v[166:169], v[214:217]
	v_fma_f32 v230, v228, s41, s41
	v_rcp_f32_e32 v227, v227
	v_mfma_f32_16x16x32_f16 v[214:217], v[46:49], v[170:173], v[214:217]
	v_fma_f32 v230, v226, v230, v230
	v_rcp_f32_e32 v230, v230
	v_mfma_f32_16x16x32_f16 v[218:221], v[18:21], v[158:161], v[218:221]
	v_fma_f32 v226, -v228, v230, v230
	v_fma_f32 v200, v200, v227, v226
	v_mfma_f32_16x16x32_f16 v[218:221], v[14:17], v[162:165], v[218:221]
	v_min_f32_e32 v226, s42, v200
	v_exp_f32_e32 v226, v226
	v_mfma_f32_16x16x32_f16 v[218:221], v[10:13], v[166:169], v[218:221]
	v_add_f32_e32 v227, 1.0, v226
	v_fma_f32 v227, v229, v227, v227
	v_mfma_f32_16x16x32_f16 v[218:221], v[26:29], v[170:173], v[218:221]
	v_rcp_f32_e32 v227, v227
	v_exp_f32_e32 v231, v214
	v_mfma_f32_16x16x32_f16 v[222:225], v[2:5], v[158:161], v[222:225]
	v_exp_f32_e32 v232, v215
	v_fma_f32 v226, -v226, v227, v227
	v_mfma_f32_16x16x32_f16 v[222:225], v[6:9], v[162:165], v[222:225]
	v_min_f32_e32 v233, s42, v216
	v_exp_f32_e32 v234, v217
	v_mfma_f32_16x16x32_f16 v[222:225], v[22:25], v[166:169], v[222:225]
	v_exp_f32_e32 v236, v218
	v_exp_f32_e32 v233, v233
	v_mfma_f32_16x16x32_f16 v[222:225], v[30:33], v[170:173], v[222:225]
	v_add_f32_e32 v232, 1.0, v232
	v_exp_f32_e32 v227, v219
	v_fma_f32 v235, v233, s41, s41
	v_rcp_f32_e32 v232, v232
	v_min_f32_e32 v228, s42, v220
	v_fma_f32 v235, v231, v235, v235
	v_rcp_f32_e32 v235, v235
	v_exp_f32_e32 v229, v221
	v_fma_f32 v231, -v233, v235, v235
	v_fma_f32 v201, v201, v232, v231
	v_exp_f32_e32 v228, v228
	v_min_f32_e32 v231, s42, v201
	v_exp_f32_e32 v231, v231
	v_add_f32_e32 v227, 1.0, v227
	v_add_f32_e32 v232, 1.0, v231
	v_mfma_f32_16x16x32_f16 v[146:149], v[122:125], v[158:161], v[146:149]
	v_fma_f32 v232, v234, v232, v232
	v_fma_f32 v230, v228, s41, s41
	v_rcp_f32_e32 v232, v232
	v_mfma_f32_16x16x32_f16 v[146:149], v[126:129], v[162:165], v[146:149]
	v_fma_f32 v231, -v231, v232, v232
	v_rcp_f32_e32 v227, v227
	v_cvt_pk_f16_f32 v246, v226, v231
	buffer_load_dwordx4 v[122:125], v189, s[76:79], s46 offen
	buffer_load_dwordx4 v[126:129], v208, s[76:79], s46 offen
	v_exp_f32_e32 v231, v222
	v_fma_f32 v230, v236, v230, v230
	v_exp_f32_e32 v232, v223
	s_waitcnt lgkmcnt(0)
	v_mfma_f32_16x16x32_f16 v[210:213], v[70:73], v[150:153], v[98:101]
	v_min_f32_e32 v233, s42, v224
	v_rcp_f32_e32 v230, v230
	v_exp_f32_e32 v234, v225
	v_mfma_f32_16x16x32_f16 v[214:217], v[74:77], v[150:153], v[102:105]
	v_exp_f32_e32 v233, v233
	v_fma_f32 v236, -v228, v230, v230
	v_add_f32_e32 v232, 1.0, v232
	v_fma_f32 v235, v233, s41, s41
	v_fma_f32 v198, v198, v227, v236
	v_rcp_f32_e32 v232, v232
	v_fma_f32 v235, v231, v235, v235
	v_min_f32_e32 v236, s42, v198
	v_rcp_f32_e32 v235, v235
	v_exp_f32_e32 v236, v236
	v_fma_f32 v231, -v233, v235, v235
	v_fma_f32 v199, v199, v232, v231
	v_min_f32_e32 v231, s42, v199
	v_add_f32_e32 v227, 1.0, v236
	v_exp_f32_e32 v231, v231
	v_fma_f32 v227, v229, v227, v227
	v_add_f32_e32 v232, 1.0, v231
	v_rcp_f32_e32 v227, v227
	v_fma_f32 v232, v234, v232, v232
	v_fma_f32 v236, -v236, v227, v227
	v_rcp_f32_e32 v232, v232
	s_nop 0
	v_fma_f32 v231, -v231, v232, v232
	v_cvt_pk_f16_f32 v247, v236, v231
	ds_write_b64 v250, v[246:247] offset:12288
	v_mfma_f32_16x16x32_f16 v[210:213], v[66:69], v[154:157], v[210:213]
	v_mfma_f32_16x16x32_f16 v[214:217], v[78:81], v[154:157], v[214:217]
	buffer_load_dwordx2 v[192:193], v209, s[56:59], s45 offen
	s_waitcnt lgkmcnt(0)
	s_barrier
	ds_read_b128 v[158:161], v248 offset:4096
	ds_read_b128 v[162:165], v248 offset:5120
	ds_read_b128 v[166:169], v249 offset:6144
	ds_read_b128 v[170:173], v249 offset:7168
	v_mfma_f32_16x16x32_f16 v[218:221], v[82:85], v[150:153], v[106:109]
	v_mfma_f32_16x16x32_f16 v[222:225], v[90:93], v[150:153], v[110:113]
	v_mfma_f32_16x16x32_f16 v[218:221], v[86:89], v[154:157], v[218:221]
	v_mfma_f32_16x16x32_f16 v[222:225], v[94:97], v[154:157], v[222:225]
	s_waitcnt lgkmcnt(2)
	v_mfma_f32_16x16x32_f16 v[210:213], v[54:57], v[158:161], v[210:213]
	v_mfma_f32_16x16x32_f16 v[210:213], v[58:61], v[162:165], v[210:213]
	s_waitcnt lgkmcnt(0)
	v_mfma_f32_16x16x32_f16 v[210:213], v[62:65], v[166:169], v[210:213]
	v_mfma_f32_16x16x32_f16 v[210:213], v[50:53], v[170:173], v[210:213]
	s_waitcnt vmcnt(9)
	v_cvt_pk_f16_f32 v251, v190, v191
	ds_write_b32 v1, v251 offset:2048
	ds_read_b128 v[150:153], v186 offset:0
	ds_read_b128 v[154:157], v186 offset:1024
	s_nop 2
	v_exp_f32_e32 v226, v210
	v_exp_f32_e32 v227, v211
	v_mfma_f32_16x16x32_f16 v[214:217], v[34:37], v[158:161], v[214:217]
	v_min_f32_e32 v228, s42, v212
	v_exp_f32_e32 v229, v213
	v_mfma_f32_16x16x32_f16 v[214:217], v[38:41], v[162:165], v[214:217]
	v_exp_f32_e32 v228, v228
	v_add_f32_e32 v227, 1.0, v227
	v_mfma_f32_16x16x32_f16 v[214:217], v[42:45], v[166:169], v[214:217]
	v_fma_f32 v230, v228, s41, s41
	v_rcp_f32_e32 v227, v227
	v_mfma_f32_16x16x32_f16 v[214:217], v[46:49], v[170:173], v[214:217]
	v_fma_f32 v230, v226, v230, v230
	v_rcp_f32_e32 v230, v230
	v_mfma_f32_16x16x32_f16 v[218:221], v[18:21], v[158:161], v[218:221]
	v_fma_f32 v226, -v228, v230, v230
	v_fma_f32 v200, v200, v227, v226
	v_mfma_f32_16x16x32_f16 v[218:221], v[14:17], v[162:165], v[218:221]
	v_min_f32_e32 v226, s42, v200
	v_exp_f32_e32 v226, v226
	v_mfma_f32_16x16x32_f16 v[218:221], v[10:13], v[166:169], v[218:221]
	v_add_f32_e32 v227, 1.0, v226
	v_fma_f32 v227, v229, v227, v227
	v_mfma_f32_16x16x32_f16 v[218:221], v[26:29], v[170:173], v[218:221]
	v_rcp_f32_e32 v227, v227
	v_exp_f32_e32 v231, v214
	v_mfma_f32_16x16x32_f16 v[222:225], v[2:5], v[158:161], v[222:225]
	v_exp_f32_e32 v232, v215
	v_fma_f32 v226, -v226, v227, v227
	v_mfma_f32_16x16x32_f16 v[222:225], v[6:9], v[162:165], v[222:225]
	v_min_f32_e32 v233, s42, v216
	v_exp_f32_e32 v234, v217
	v_mfma_f32_16x16x32_f16 v[222:225], v[22:25], v[166:169], v[222:225]
	v_exp_f32_e32 v236, v218
	v_exp_f32_e32 v233, v233
	v_mfma_f32_16x16x32_f16 v[222:225], v[30:33], v[170:173], v[222:225]
	v_add_f32_e32 v232, 1.0, v232
	v_exp_f32_e32 v227, v219
	v_fma_f32 v235, v233, s41, s41
	v_rcp_f32_e32 v232, v232
	v_min_f32_e32 v228, s42, v220
	v_fma_f32 v235, v231, v235, v235
	v_rcp_f32_e32 v235, v235
	v_exp_f32_e32 v229, v221
	v_fma_f32 v231, -v233, v235, v235
	v_fma_f32 v201, v201, v232, v231
	v_exp_f32_e32 v228, v228
	v_min_f32_e32 v231, s42, v201
	v_exp_f32_e32 v231, v231
	v_add_f32_e32 v227, 1.0, v227
	v_add_f32_e32 v232, 1.0, v231
	v_mfma_f32_16x16x32_f16 v[146:149], v[114:117], v[158:161], v[146:149]
	v_fma_f32 v232, v234, v232, v232
	v_fma_f32 v230, v228, s41, s41
	v_rcp_f32_e32 v232, v232
	v_mfma_f32_16x16x32_f16 v[146:149], v[118:121], v[162:165], v[146:149]
	v_fma_f32 v231, -v231, v232, v232
	v_rcp_f32_e32 v227, v227
	v_cvt_pk_f16_f32 v246, v226, v231
	buffer_load_dwordx4 v[114:117], v189, s[80:83], s46 offen
	buffer_load_dwordx4 v[118:121], v208, s[80:83], s46 offen
	v_exp_f32_e32 v231, v222
	v_fma_f32 v230, v236, v230, v230
	v_exp_f32_e32 v232, v223
	s_waitcnt lgkmcnt(0)
	v_mfma_f32_16x16x32_f16 v[210:213], v[70:73], v[150:153], v[98:101]
	v_min_f32_e32 v233, s42, v224
	v_rcp_f32_e32 v230, v230
	v_exp_f32_e32 v234, v225
	v_mfma_f32_16x16x32_f16 v[214:217], v[74:77], v[150:153], v[102:105]
	v_exp_f32_e32 v233, v233
	v_fma_f32 v236, -v228, v230, v230
	v_add_f32_e32 v232, 1.0, v232
	v_fma_f32 v235, v233, s41, s41
	v_fma_f32 v198, v198, v227, v236
	v_rcp_f32_e32 v232, v232
	v_fma_f32 v235, v231, v235, v235
	v_min_f32_e32 v236, s42, v198
	v_rcp_f32_e32 v235, v235
	v_exp_f32_e32 v236, v236
	v_fma_f32 v231, -v233, v235, v235
	v_fma_f32 v199, v199, v232, v231
	v_min_f32_e32 v231, s42, v199
	v_add_f32_e32 v227, 1.0, v236
	v_exp_f32_e32 v231, v231
	v_fma_f32 v227, v229, v227, v227
	v_add_f32_e32 v232, 1.0, v231
	v_rcp_f32_e32 v227, v227
	v_fma_f32 v232, v234, v232, v232
	v_fma_f32 v236, -v236, v227, v227
	v_rcp_f32_e32 v232, v232
	s_nop 0
	v_fma_f32 v231, -v231, v232, v232
	v_cvt_pk_f16_f32 v247, v236, v231
	ds_write_b64 v250, v[246:247] offset:16384
	v_mfma_f32_16x16x32_f16 v[210:213], v[66:69], v[154:157], v[210:213]
	v_mfma_f32_16x16x32_f16 v[214:217], v[78:81], v[154:157], v[214:217]
	buffer_load_dwordx2 v[190:191], v209, s[60:63], s45 offen
	s_add_i32 s45, s45, 0x400000
	s_add_i32 s46, s46, 0x10000
	s_waitcnt lgkmcnt(0)
	s_barrier
	ds_read_b128 v[158:161], v248 offset:8192
	ds_read_b128 v[162:165], v248 offset:9216
	ds_read_b128 v[166:169], v249 offset:10240
	ds_read_b128 v[170:173], v249 offset:11264
	v_mfma_f32_16x16x32_f16 v[218:221], v[82:85], v[150:153], v[106:109]
	v_mfma_f32_16x16x32_f16 v[222:225], v[90:93], v[150:153], v[110:113]
	v_mfma_f32_16x16x32_f16 v[218:221], v[86:89], v[154:157], v[218:221]
	v_mfma_f32_16x16x32_f16 v[222:225], v[94:97], v[154:157], v[222:225]
	s_waitcnt lgkmcnt(2)
	v_mfma_f32_16x16x32_f16 v[210:213], v[54:57], v[158:161], v[210:213]
	v_mfma_f32_16x16x32_f16 v[210:213], v[58:61], v[162:165], v[210:213]
	s_waitcnt lgkmcnt(0)
	v_mfma_f32_16x16x32_f16 v[210:213], v[62:65], v[166:169], v[210:213]
	v_mfma_f32_16x16x32_f16 v[210:213], v[50:53], v[170:173], v[210:213]
	s_waitcnt vmcnt(9)
	v_cvt_pk_f16_f32 v251, v196, v197
	ds_write_b32 v1, v251 offset:4096
	ds_read_b128 v[150:153], v186 offset:2048
	ds_read_b128 v[154:157], v186 offset:3072
	s_nop 2
	v_exp_f32_e32 v226, v210
	v_exp_f32_e32 v227, v211
	v_mfma_f32_16x16x32_f16 v[214:217], v[34:37], v[158:161], v[214:217]
	v_min_f32_e32 v228, s42, v212
	v_exp_f32_e32 v229, v213
	v_mfma_f32_16x16x32_f16 v[214:217], v[38:41], v[162:165], v[214:217]
	v_exp_f32_e32 v228, v228
	v_add_f32_e32 v227, 1.0, v227
	v_mfma_f32_16x16x32_f16 v[214:217], v[42:45], v[166:169], v[214:217]
	v_fma_f32 v230, v228, s41, s41
	v_rcp_f32_e32 v227, v227
	v_mfma_f32_16x16x32_f16 v[214:217], v[46:49], v[170:173], v[214:217]
	v_fma_f32 v230, v226, v230, v230
	v_rcp_f32_e32 v230, v230
	v_mfma_f32_16x16x32_f16 v[218:221], v[18:21], v[158:161], v[218:221]
	v_fma_f32 v226, -v228, v230, v230
	v_fma_f32 v200, v200, v227, v226
	v_mfma_f32_16x16x32_f16 v[218:221], v[14:17], v[162:165], v[218:221]
	v_min_f32_e32 v226, s42, v200
	v_exp_f32_e32 v226, v226
	v_mfma_f32_16x16x32_f16 v[218:221], v[10:13], v[166:169], v[218:221]
	v_add_f32_e32 v227, 1.0, v226
	v_fma_f32 v227, v229, v227, v227
	v_mfma_f32_16x16x32_f16 v[218:221], v[26:29], v[170:173], v[218:221]
	v_rcp_f32_e32 v227, v227
	v_exp_f32_e32 v231, v214
	v_mfma_f32_16x16x32_f16 v[222:225], v[2:5], v[158:161], v[222:225]
	v_exp_f32_e32 v232, v215
	v_fma_f32 v226, -v226, v227, v227
	v_mfma_f32_16x16x32_f16 v[222:225], v[6:9], v[162:165], v[222:225]
	v_min_f32_e32 v233, s42, v216
	v_exp_f32_e32 v234, v217
	v_mfma_f32_16x16x32_f16 v[222:225], v[22:25], v[166:169], v[222:225]
	v_exp_f32_e32 v236, v218
	v_exp_f32_e32 v233, v233
	v_mfma_f32_16x16x32_f16 v[222:225], v[30:33], v[170:173], v[222:225]
	v_add_f32_e32 v232, 1.0, v232
	v_exp_f32_e32 v227, v219
	v_fma_f32 v235, v233, s41, s41
	v_rcp_f32_e32 v232, v232
	v_min_f32_e32 v228, s42, v220
	v_fma_f32 v235, v231, v235, v235
	v_rcp_f32_e32 v235, v235
	v_exp_f32_e32 v229, v221
	v_fma_f32 v231, -v233, v235, v235
	v_fma_f32 v201, v201, v232, v231
	v_exp_f32_e32 v228, v228
	v_min_f32_e32 v231, s42, v201
	v_exp_f32_e32 v231, v231
	v_add_f32_e32 v227, 1.0, v227
	v_add_f32_e32 v232, 1.0, v231
	v_mfma_f32_16x16x32_f16 v[146:149], v[138:141], v[158:161], v[146:149]
	v_fma_f32 v232, v234, v232, v232
	v_fma_f32 v230, v228, s41, s41
	v_rcp_f32_e32 v232, v232
	v_mfma_f32_16x16x32_f16 v[146:149], v[142:145], v[162:165], v[146:149]
	v_fma_f32 v231, -v231, v232, v232
	v_rcp_f32_e32 v227, v227
	v_cvt_pk_f16_f32 v246, v226, v231
	buffer_load_dwordx4 v[138:141], v189, s[68:71], s46 offen
	buffer_load_dwordx4 v[142:145], v208, s[68:71], s46 offen
	v_exp_f32_e32 v231, v222
	v_fma_f32 v230, v236, v230, v230
	v_exp_f32_e32 v232, v223
	s_waitcnt lgkmcnt(0)
	v_mfma_f32_16x16x32_f16 v[210:213], v[70:73], v[150:153], v[98:101]
	v_min_f32_e32 v233, s42, v224
	v_rcp_f32_e32 v230, v230
	v_exp_f32_e32 v234, v225
	v_mfma_f32_16x16x32_f16 v[214:217], v[74:77], v[150:153], v[102:105]
	v_exp_f32_e32 v233, v233
	v_fma_f32 v236, -v228, v230, v230
	v_add_f32_e32 v232, 1.0, v232
	v_fma_f32 v235, v233, s41, s41
	v_fma_f32 v198, v198, v227, v236
	v_rcp_f32_e32 v232, v232
	v_fma_f32 v235, v231, v235, v235
	v_min_f32_e32 v236, s42, v198
	v_rcp_f32_e32 v235, v235
	v_exp_f32_e32 v236, v236
	v_fma_f32 v231, -v233, v235, v235
	v_fma_f32 v199, v199, v232, v231
	v_min_f32_e32 v231, s42, v199
	v_add_f32_e32 v227, 1.0, v236
	v_exp_f32_e32 v231, v231
	v_fma_f32 v227, v229, v227, v227
	v_add_f32_e32 v232, 1.0, v231
	v_rcp_f32_e32 v227, v227
	v_fma_f32 v232, v234, v232, v232
	v_fma_f32 v236, -v236, v227, v227
	v_rcp_f32_e32 v232, v232
	s_nop 0
	v_fma_f32 v231, -v231, v232, v232
	v_cvt_pk_f16_f32 v247, v236, v231
	ds_write_b64 v250, v[246:247] offset:20480
	v_mfma_f32_16x16x32_f16 v[210:213], v[66:69], v[154:157], v[210:213]
	v_mfma_f32_16x16x32_f16 v[214:217], v[78:81], v[154:157], v[214:217]
	buffer_load_dwordx2 v[196:197], v209, s[48:51], s45 offen
	s_waitcnt lgkmcnt(0)
	s_barrier
	ds_read_b128 v[158:161], v248 offset:12288
	ds_read_b128 v[162:165], v248 offset:13312
	ds_read_b128 v[166:169], v249 offset:14336
	ds_read_b128 v[170:173], v249 offset:15360
	v_mfma_f32_16x16x32_f16 v[218:221], v[82:85], v[150:153], v[106:109]
	v_mfma_f32_16x16x32_f16 v[222:225], v[90:93], v[150:153], v[110:113]
	v_mfma_f32_16x16x32_f16 v[218:221], v[86:89], v[154:157], v[218:221]
	v_mfma_f32_16x16x32_f16 v[222:225], v[94:97], v[154:157], v[222:225]
	s_waitcnt lgkmcnt(2)
	v_mfma_f32_16x16x32_f16 v[210:213], v[54:57], v[158:161], v[210:213]
	v_mfma_f32_16x16x32_f16 v[210:213], v[58:61], v[162:165], v[210:213]
	s_waitcnt lgkmcnt(0)
	v_mfma_f32_16x16x32_f16 v[210:213], v[62:65], v[166:169], v[210:213]
	v_mfma_f32_16x16x32_f16 v[210:213], v[50:53], v[170:173], v[210:213]
	s_waitcnt vmcnt(9)
	v_cvt_pk_f16_f32 v251, v194, v195
	ds_write_b32 v1, v251 offset:6144
	ds_read_b128 v[150:153], v186 offset:4096
	ds_read_b128 v[154:157], v186 offset:5120
	s_nop 2
	v_exp_f32_e32 v226, v210
	v_exp_f32_e32 v227, v211
	v_mfma_f32_16x16x32_f16 v[214:217], v[34:37], v[158:161], v[214:217]
	v_min_f32_e32 v228, s42, v212
	v_exp_f32_e32 v229, v213
	v_mfma_f32_16x16x32_f16 v[214:217], v[38:41], v[162:165], v[214:217]
	v_exp_f32_e32 v228, v228
	v_add_f32_e32 v227, 1.0, v227
	v_mfma_f32_16x16x32_f16 v[214:217], v[42:45], v[166:169], v[214:217]
	v_fma_f32 v230, v228, s41, s41
	v_rcp_f32_e32 v227, v227
	v_mfma_f32_16x16x32_f16 v[214:217], v[46:49], v[170:173], v[214:217]
	v_fma_f32 v230, v226, v230, v230
	v_rcp_f32_e32 v230, v230
	v_mfma_f32_16x16x32_f16 v[218:221], v[18:21], v[158:161], v[218:221]
	v_fma_f32 v226, -v228, v230, v230
	v_fma_f32 v200, v200, v227, v226
	v_mfma_f32_16x16x32_f16 v[218:221], v[14:17], v[162:165], v[218:221]
	v_min_f32_e32 v226, s42, v200
	v_exp_f32_e32 v226, v226
	v_mfma_f32_16x16x32_f16 v[218:221], v[10:13], v[166:169], v[218:221]
	v_add_f32_e32 v227, 1.0, v226
	v_fma_f32 v227, v229, v227, v227
	v_mfma_f32_16x16x32_f16 v[218:221], v[26:29], v[170:173], v[218:221]
	v_rcp_f32_e32 v227, v227
	v_exp_f32_e32 v231, v214
	v_mfma_f32_16x16x32_f16 v[222:225], v[2:5], v[158:161], v[222:225]
	v_exp_f32_e32 v232, v215
	v_fma_f32 v226, -v226, v227, v227
	v_mfma_f32_16x16x32_f16 v[222:225], v[6:9], v[162:165], v[222:225]
	v_min_f32_e32 v233, s42, v216
	v_exp_f32_e32 v234, v217
	v_mfma_f32_16x16x32_f16 v[222:225], v[22:25], v[166:169], v[222:225]
	v_exp_f32_e32 v236, v218
	v_exp_f32_e32 v233, v233
	v_mfma_f32_16x16x32_f16 v[222:225], v[30:33], v[170:173], v[222:225]
	v_add_f32_e32 v232, 1.0, v232
	v_exp_f32_e32 v227, v219
	v_fma_f32 v235, v233, s41, s41
	v_rcp_f32_e32 v232, v232
	v_min_f32_e32 v228, s42, v220
	v_fma_f32 v235, v231, v235, v235
	v_rcp_f32_e32 v235, v235
	v_exp_f32_e32 v229, v221
	v_fma_f32 v231, -v233, v235, v235
	v_fma_f32 v201, v201, v232, v231
	v_exp_f32_e32 v228, v228
	v_min_f32_e32 v231, s42, v201
	v_exp_f32_e32 v231, v231
	v_add_f32_e32 v227, 1.0, v227
	v_add_f32_e32 v232, 1.0, v231
	v_mfma_f32_16x16x32_f16 v[146:149], v[130:133], v[158:161], v[146:149]
	v_fma_f32 v232, v234, v232, v232
	v_fma_f32 v230, v228, s41, s41
	v_rcp_f32_e32 v232, v232
	v_mfma_f32_16x16x32_f16 v[146:149], v[134:137], v[162:165], v[146:149]
	v_fma_f32 v231, -v231, v232, v232
	v_rcp_f32_e32 v227, v227
	v_cvt_pk_f16_f32 v246, v226, v231
	buffer_load_dwordx4 v[130:133], v189, s[72:75], s46 offen
	buffer_load_dwordx4 v[134:137], v208, s[72:75], s46 offen
	v_exp_f32_e32 v231, v222
	v_fma_f32 v230, v236, v230, v230
	v_exp_f32_e32 v232, v223
	s_waitcnt lgkmcnt(0)
	v_mfma_f32_16x16x32_f16 v[210:213], v[70:73], v[150:153], v[98:101]
	v_min_f32_e32 v233, s42, v224
	v_rcp_f32_e32 v230, v230
	v_exp_f32_e32 v234, v225
	v_mfma_f32_16x16x32_f16 v[214:217], v[74:77], v[150:153], v[102:105]
	v_exp_f32_e32 v233, v233
	v_fma_f32 v236, -v228, v230, v230
	v_add_f32_e32 v232, 1.0, v232
	v_fma_f32 v235, v233, s41, s41
	v_fma_f32 v198, v198, v227, v236
	v_rcp_f32_e32 v232, v232
	v_fma_f32 v235, v231, v235, v235
	v_min_f32_e32 v236, s42, v198
	v_rcp_f32_e32 v235, v235
	v_exp_f32_e32 v236, v236
	v_fma_f32 v231, -v233, v235, v235
	v_fma_f32 v199, v199, v232, v231
	v_min_f32_e32 v231, s42, v199
	v_add_f32_e32 v227, 1.0, v236
	v_exp_f32_e32 v231, v231
	v_fma_f32 v227, v229, v227, v227
	v_add_f32_e32 v232, 1.0, v231
	v_rcp_f32_e32 v227, v227
	v_fma_f32 v232, v234, v232, v232
	v_fma_f32 v236, -v236, v227, v227
	v_rcp_f32_e32 v232, v232
	s_nop 0
	v_fma_f32 v231, -v231, v232, v232
	v_cvt_pk_f16_f32 v247, v236, v231
	ds_write_b64 v250, v[246:247] offset:24576
	v_mfma_f32_16x16x32_f16 v[210:213], v[66:69], v[154:157], v[210:213]
	v_mfma_f32_16x16x32_f16 v[214:217], v[78:81], v[154:157], v[214:217]
	buffer_load_dwordx2 v[194:195], v209, s[52:55], s45 offen
	v_add_u32_e32 v250, 0x4000, v250
	v_add_u32_e32 v248, 0x4000, v248
	v_add_u32_e32 v249, 0x4000, v249
	s_waitcnt lgkmcnt(0)
	s_barrier
	s_nop 7
	ds_read_b128 v[158:161], v248 offset:0
	ds_read_b128 v[162:165], v248 offset:1024
	s_lshr_b32 s48, s35, 5
	v_and_b32_e32 v211, 15, v0
	v_bfe_u32 v212, v0, 4, 2
	v_and_b32_e32 v213, 31, v0
	v_bfe_u32 v214, v0, 5, 1
	v_add_u32_e32 v214, s48, v214
	s_lshl_b32 s49, s35, 4
	s_addk_i32 s49, 0x2000
	v_lshl_add_u32 v215, v212, 8, s49
	v_lshl_add_u32 v215, v211, 2, v215
	v_lshlrev_b32_e32 v216, 6, v213
	v_lshl_add_u32 v216, v214, 2, v216
	v_mul_u32_u24_e32 v217, 0x110, v214
	v_lshl_add_u32 v217, v213, 2, v217
	v_mul_u32_u24_e32 v218, 0x110, v211
	v_add_u32_e32 v219, 0x4000, v206
	v_add_u32_e32 v220, 0x14000, v206
	v_add_u32_e32 v221, 0x24000, v206
	v_add_u32_e32 v222, s34, v211
	v_lshlrev_b32_e32 v222, 9, v222
	v_add_u32_e32 v222, s35, v222
	v_lshl_add_u32 v222, v212, 4, v222
	s_waitcnt vmcnt(10) lgkmcnt(0)
	v_mfma_f32_16x16x32_f16 v[146:149], v[122:125], v[158:161], v[146:149]
	v_mfma_f32_16x16x32_f16 v[146:149], v[126:129], v[162:165], v[146:149]
	ds_read_b64 v[30:31], v219 offset:0
	ds_read_b64 v[32:33], v219 offset:4096
	ds_read_b64 v[34:35], v219 offset:8192
	ds_read_b64 v[36:37], v219 offset:12288
	ds_read_b64 v[38:39], v219 offset:16384
	ds_read_b64 v[40:41], v219 offset:20480
	ds_read_b64 v[42:43], v219 offset:24576
	ds_read_b64 v[44:45], v219 offset:28672
	s_waitcnt lgkmcnt(4)
	ds_read_b64 v[46:47], v219 offset:32768
	ds_read_b64 v[48:49], v219 offset:36864
	ds_read_b64 v[50:51], v219 offset:40960
	ds_read_b64 v[52:53], v219 offset:45056
	ds_read_b64 v[54:55], v219 offset:49152
	ds_read_b64 v[56:57], v219 offset:53248
	ds_read_b64 v[58:59], v219 offset:57344
	ds_read_b64 v[60:61], v219 offset:61440
	s_waitcnt lgkmcnt(4)
	ds_read_b64 v[62:63], v220 offset:0
	ds_read_b64 v[64:65], v220 offset:4096
	ds_read_b64 v[66:67], v220 offset:8192
	ds_read_b64 v[68:69], v220 offset:12288
	ds_read_b64 v[70:71], v220 offset:16384
	ds_read_b64 v[72:73], v220 offset:20480
	ds_read_b64 v[74:75], v220 offset:24576
	ds_read_b64 v[76:77], v220 offset:28672
	s_waitcnt lgkmcnt(4)
	ds_read_b64 v[78:79], v220 offset:32768
	ds_read_b64 v[80:81], v220 offset:36864
	ds_read_b64 v[82:83], v220 offset:40960
	ds_read_b64 v[84:85], v220 offset:45056
	ds_read_b64 v[86:87], v220 offset:49152
	ds_read_b64 v[88:89], v220 offset:53248
	ds_read_b64 v[90:91], v220 offset:57344
	ds_read_b64 v[92:93], v220 offset:61440
	s_waitcnt lgkmcnt(4)
	ds_read_b64 v[94:95], v221 offset:0
	ds_read_b64 v[96:97], v221 offset:4096
	ds_read_b64 v[98:99], v221 offset:8192
	ds_read_b64 v[100:101], v221 offset:12288
	ds_write2_b32 v215, v146, v147 offset1:16
	ds_write2_b32 v215, v148, v149 offset0:32 offset1:48
	s_waitcnt lgkmcnt(0)
	s_barrier
	ds_read2st64_b32 v[230:231], v216 offset0:32 offset1:48
	ds_read2st64_b32 v[232:233], v216 offset0:40 offset1:56
	v_cmp_gt_u32_e32 vcc, 18, v213
	s_waitcnt vmcnt(0) lgkmcnt(0)
	v_add_f32_e32 v223, v230, v231
	v_add_f32_e32 v224, v232, v233
	v_add_f32_e32 v223, v223, v254
	v_add_f32_e32 v224, v224, v255
	v_max_f32_e32 v223, 0, v223
	v_max_f32_e32 v224, 0, v224
	v_mov_b32_e32 v226, 0xf149f2ca
	v_cndmask_b32_e32 v224, v226, v224, vcc
	v_max_f32_e32 v225, v223, v224
	s_nop 1
	v_max_f32_dpp v226, v225, v225 quad_perm:[1,0,3,2] row_mask:0xf bank_mask:0xf
	s_nop 1
	v_max_f32_dpp v225, v226, v226 quad_perm:[2,3,0,1] row_mask:0xf bank_mask:0xf
	s_nop 1
	v_max_f32_dpp v226, v225, v225 row_half_mirror row_mask:0xf bank_mask:0xf
	s_nop 1
	v_max_f32_dpp v225, v226, v226 row_mirror row_mask:0xf bank_mask:0xf
	ds_swizzle_b32 v226, v225 offset:swizzle(SWAP,16)
	s_waitcnt lgkmcnt(0)
	v_max_f32_e32 v225, v225, v226
	v_sub_f32_e32 v223, v223, v225
	v_sub_f32_e32 v224, v224, v225
	v_mul_f32_e32 v223, 0x3fb8aa3b, v223
	v_mul_f32_e32 v224, 0x3fb8aa3b, v224
	v_exp_f32_e32 v227, v223
	v_exp_f32_e32 v228, v224
	s_nop 0
	v_add_f32_e32 v229, v227, v228
	s_nop 1
	v_add_f32_dpp v226, v229, v229 quad_perm:[1,0,3,2] row_mask:0xf bank_mask:0xf
	s_nop 1
	v_add_f32_dpp v229, v226, v226 quad_perm:[2,3,0,1] row_mask:0xf bank_mask:0xf
	s_nop 1
	v_add_f32_dpp v226, v229, v229 row_half_mirror row_mask:0xf bank_mask:0xf
	s_nop 1
	v_add_f32_dpp v229, v226, v226 row_mirror row_mask:0xf bank_mask:0xf
	ds_swizzle_b32 v226, v229 offset:swizzle(SWAP,16)
	s_waitcnt lgkmcnt(0)
	v_add_f32_e32 v229, v229, v226
	v_rcp_f32_e32 v234, v229
	s_nop 0
	v_mul_f32_e32 v227, v227, v234
	v_mul_f32_e32 v228, v228, v234
	ds_write_b32 v217, v227
	ds_write_b32 v217, v228 offset:128
	s_waitcnt lgkmcnt(0)
	s_barrier
	ds_read_b128 v[102:105], v218 offset:0
	ds_read_b128 v[106:109], v218 offset:16
	ds_read_b128 v[110:113], v218 offset:32
	ds_read_b128 v[114:117], v218 offset:48
	ds_read_b128 v[118:121], v218 offset:64
	ds_read_b128 v[122:125], v218 offset:80
	ds_read_b128 v[126:129], v218 offset:96
	ds_read_b128 v[130:133], v218 offset:112
	ds_read_b128 v[134:137], v218 offset:128
	ds_read_b128 v[138:141], v218 offset:144
	ds_read_b128 v[142:145], v218 offset:160
	ds_read_b128 v[146:149], v218 offset:176
	ds_read_b128 v[150:153], v218 offset:192
	v_mov_b32_e32 v154, 0
	v_mov_b32_e32 v155, 0
	v_mov_b32_e32 v156, 0
	v_mov_b32_e32 v157, 0
	s_waitcnt vmcnt(0) lgkmcnt(0)
	v_fma_mix_f32 v154, v174, v102, v154 op_sel_hi:[1,0,0]
	v_fma_mix_f32 v155, v174, v102, v155 op_sel:[1,0,0] op_sel_hi:[1,0,0]
	v_fma_mix_f32 v156, v175, v102, v156 op_sel_hi:[1,0,0]
	v_fma_mix_f32 v157, v175, v102, v157 op_sel:[1,0,0] op_sel_hi:[1,0,0]
	v_fma_mix_f32 v154, v176, v103, v154 op_sel_hi:[1,0,0]
	v_fma_mix_f32 v155, v176, v103, v155 op_sel:[1,0,0] op_sel_hi:[1,0,0]
	v_fma_mix_f32 v156, v177, v103, v156 op_sel_hi:[1,0,0]
	v_fma_mix_f32 v157, v177, v103, v157 op_sel:[1,0,0] op_sel_hi:[1,0,0]
	v_fma_mix_f32 v154, v178, v104, v154 op_sel_hi:[1,0,0]
	v_fma_mix_f32 v155, v178, v104, v155 op_sel:[1,0,0] op_sel_hi:[1,0,0]
	v_fma_mix_f32 v156, v179, v104, v156 op_sel_hi:[1,0,0]
	v_fma_mix_f32 v157, v179, v104, v157 op_sel:[1,0,0] op_sel_hi:[1,0,0]
	v_fma_mix_f32 v154, v180, v105, v154 op_sel_hi:[1,0,0]
	v_fma_mix_f32 v155, v180, v105, v155 op_sel:[1,0,0] op_sel_hi:[1,0,0]
	v_fma_mix_f32 v156, v181, v105, v156 op_sel_hi:[1,0,0]
	v_fma_mix_f32 v157, v181, v105, v157 op_sel:[1,0,0] op_sel_hi:[1,0,0]
	v_fma_mix_f32 v154, v182, v106, v154 op_sel_hi:[1,0,0]
	v_fma_mix_f32 v155, v182, v106, v155 op_sel:[1,0,0] op_sel_hi:[1,0,0]
	v_fma_mix_f32 v156, v183, v106, v156 op_sel_hi:[1,0,0]
	v_fma_mix_f32 v157, v183, v106, v157 op_sel:[1,0,0] op_sel_hi:[1,0,0]
	v_fma_mix_f32 v154, v184, v107, v154 op_sel_hi:[1,0,0]
	v_fma_mix_f32 v155, v184, v107, v155 op_sel:[1,0,0] op_sel_hi:[1,0,0]
	v_fma_mix_f32 v156, v185, v107, v156 op_sel_hi:[1,0,0]
	v_fma_mix_f32 v157, v185, v107, v157 op_sel:[1,0,0] op_sel_hi:[1,0,0]
	v_fma_mix_f32 v154, v237, v108, v154 op_sel_hi:[1,0,0]
	v_fma_mix_f32 v155, v237, v108, v155 op_sel:[1,0,0] op_sel_hi:[1,0,0]
	v_fma_mix_f32 v156, v238, v108, v156 op_sel_hi:[1,0,0]
	v_fma_mix_f32 v157, v238, v108, v157 op_sel:[1,0,0] op_sel_hi:[1,0,0]
	v_fma_mix_f32 v154, v239, v109, v154 op_sel_hi:[1,0,0]
	v_fma_mix_f32 v155, v239, v109, v155 op_sel:[1,0,0] op_sel_hi:[1,0,0]
	v_fma_mix_f32 v156, v240, v109, v156 op_sel_hi:[1,0,0]
	v_fma_mix_f32 v157, v240, v109, v157 op_sel:[1,0,0] op_sel_hi:[1,0,0]
	v_fma_mix_f32 v154, v241, v110, v154 op_sel_hi:[1,0,0]
	v_fma_mix_f32 v155, v241, v110, v155 op_sel:[1,0,0] op_sel_hi:[1,0,0]
	v_fma_mix_f32 v156, v242, v110, v156 op_sel_hi:[1,0,0]
	v_fma_mix_f32 v157, v242, v110, v157 op_sel:[1,0,0] op_sel_hi:[1,0,0]
	v_fma_mix_f32 v154, v243, v111, v154 op_sel_hi:[1,0,0]
	v_fma_mix_f32 v155, v243, v111, v155 op_sel:[1,0,0] op_sel_hi:[1,0,0]
	v_fma_mix_f32 v156, v244, v111, v156 op_sel_hi:[1,0,0]
	v_fma_mix_f32 v157, v244, v111, v157 op_sel:[1,0,0] op_sel_hi:[1,0,0]
	v_fma_mix_f32 v154, v245, v112, v154 op_sel_hi:[1,0,0]
	v_fma_mix_f32 v155, v245, v112, v155 op_sel:[1,0,0] op_sel_hi:[1,0,0]
	v_fma_mix_f32 v156, v187, v112, v156 op_sel_hi:[1,0,0]
	v_fma_mix_f32 v157, v187, v112, v157 op_sel:[1,0,0] op_sel_hi:[1,0,0]
	v_fma_mix_f32 v154, v188, v113, v154 op_sel_hi:[1,0,0]
	v_fma_mix_f32 v155, v188, v113, v155 op_sel:[1,0,0] op_sel_hi:[1,0,0]
	v_fma_mix_f32 v156, v202, v113, v156 op_sel_hi:[1,0,0]
	v_fma_mix_f32 v157, v202, v113, v157 op_sel:[1,0,0] op_sel_hi:[1,0,0]
	v_fma_mix_f32 v154, v203, v114, v154 op_sel_hi:[1,0,0]
	v_fma_mix_f32 v155, v203, v114, v155 op_sel:[1,0,0] op_sel_hi:[1,0,0]
	v_fma_mix_f32 v156, v204, v114, v156 op_sel_hi:[1,0,0]
	v_fma_mix_f32 v157, v204, v114, v157 op_sel:[1,0,0] op_sel_hi:[1,0,0]
	v_fma_mix_f32 v154, v205, v115, v154 op_sel_hi:[1,0,0]
	v_fma_mix_f32 v155, v205, v115, v155 op_sel:[1,0,0] op_sel_hi:[1,0,0]
	v_fma_mix_f32 v156, v207, v115, v156 op_sel_hi:[1,0,0]
	v_fma_mix_f32 v157, v207, v115, v157 op_sel:[1,0,0] op_sel_hi:[1,0,0]
	v_fma_mix_f32 v154, v30, v116, v154 op_sel_hi:[1,0,0]
	v_fma_mix_f32 v155, v30, v116, v155 op_sel:[1,0,0] op_sel_hi:[1,0,0]
	v_fma_mix_f32 v156, v31, v116, v156 op_sel_hi:[1,0,0]
	v_fma_mix_f32 v157, v31, v116, v157 op_sel:[1,0,0] op_sel_hi:[1,0,0]
	v_fma_mix_f32 v154, v32, v117, v154 op_sel_hi:[1,0,0]
	v_fma_mix_f32 v155, v32, v117, v155 op_sel:[1,0,0] op_sel_hi:[1,0,0]
	v_fma_mix_f32 v156, v33, v117, v156 op_sel_hi:[1,0,0]
	v_fma_mix_f32 v157, v33, v117, v157 op_sel:[1,0,0] op_sel_hi:[1,0,0]
	v_fma_mix_f32 v154, v34, v118, v154 op_sel_hi:[1,0,0]
	v_fma_mix_f32 v155, v34, v118, v155 op_sel:[1,0,0] op_sel_hi:[1,0,0]
	v_fma_mix_f32 v156, v35, v118, v156 op_sel_hi:[1,0,0]
	v_fma_mix_f32 v157, v35, v118, v157 op_sel:[1,0,0] op_sel_hi:[1,0,0]
	v_fma_mix_f32 v154, v36, v119, v154 op_sel_hi:[1,0,0]
	v_fma_mix_f32 v155, v36, v119, v155 op_sel:[1,0,0] op_sel_hi:[1,0,0]
	v_fma_mix_f32 v156, v37, v119, v156 op_sel_hi:[1,0,0]
	v_fma_mix_f32 v157, v37, v119, v157 op_sel:[1,0,0] op_sel_hi:[1,0,0]
	v_fma_mix_f32 v154, v38, v120, v154 op_sel_hi:[1,0,0]
	v_fma_mix_f32 v155, v38, v120, v155 op_sel:[1,0,0] op_sel_hi:[1,0,0]
	v_fma_mix_f32 v156, v39, v120, v156 op_sel_hi:[1,0,0]
	v_fma_mix_f32 v157, v39, v120, v157 op_sel:[1,0,0] op_sel_hi:[1,0,0]
	v_fma_mix_f32 v154, v40, v121, v154 op_sel_hi:[1,0,0]
	v_fma_mix_f32 v155, v40, v121, v155 op_sel:[1,0,0] op_sel_hi:[1,0,0]
	v_fma_mix_f32 v156, v41, v121, v156 op_sel_hi:[1,0,0]
	v_fma_mix_f32 v157, v41, v121, v157 op_sel:[1,0,0] op_sel_hi:[1,0,0]
	v_fma_mix_f32 v154, v42, v122, v154 op_sel_hi:[1,0,0]
	v_fma_mix_f32 v155, v42, v122, v155 op_sel:[1,0,0] op_sel_hi:[1,0,0]
	v_fma_mix_f32 v156, v43, v122, v156 op_sel_hi:[1,0,0]
	v_fma_mix_f32 v157, v43, v122, v157 op_sel:[1,0,0] op_sel_hi:[1,0,0]
	v_fma_mix_f32 v154, v44, v123, v154 op_sel_hi:[1,0,0]
	v_fma_mix_f32 v155, v44, v123, v155 op_sel:[1,0,0] op_sel_hi:[1,0,0]
	v_fma_mix_f32 v156, v45, v123, v156 op_sel_hi:[1,0,0]
	v_fma_mix_f32 v157, v45, v123, v157 op_sel:[1,0,0] op_sel_hi:[1,0,0]
	v_fma_mix_f32 v154, v46, v124, v154 op_sel_hi:[1,0,0]
	v_fma_mix_f32 v155, v46, v124, v155 op_sel:[1,0,0] op_sel_hi:[1,0,0]
	v_fma_mix_f32 v156, v47, v124, v156 op_sel_hi:[1,0,0]
	v_fma_mix_f32 v157, v47, v124, v157 op_sel:[1,0,0] op_sel_hi:[1,0,0]
	v_fma_mix_f32 v154, v48, v125, v154 op_sel_hi:[1,0,0]
	v_fma_mix_f32 v155, v48, v125, v155 op_sel:[1,0,0] op_sel_hi:[1,0,0]
	v_fma_mix_f32 v156, v49, v125, v156 op_sel_hi:[1,0,0]
	v_fma_mix_f32 v157, v49, v125, v157 op_sel:[1,0,0] op_sel_hi:[1,0,0]
	v_fma_mix_f32 v154, v50, v126, v154 op_sel_hi:[1,0,0]
	v_fma_mix_f32 v155, v50, v126, v155 op_sel:[1,0,0] op_sel_hi:[1,0,0]
	v_fma_mix_f32 v156, v51, v126, v156 op_sel_hi:[1,0,0]
	v_fma_mix_f32 v157, v51, v126, v157 op_sel:[1,0,0] op_sel_hi:[1,0,0]
	v_fma_mix_f32 v154, v52, v127, v154 op_sel_hi:[1,0,0]
	v_fma_mix_f32 v155, v52, v127, v155 op_sel:[1,0,0] op_sel_hi:[1,0,0]
	v_fma_mix_f32 v156, v53, v127, v156 op_sel_hi:[1,0,0]
	v_fma_mix_f32 v157, v53, v127, v157 op_sel:[1,0,0] op_sel_hi:[1,0,0]
	v_fma_mix_f32 v154, v54, v128, v154 op_sel_hi:[1,0,0]
	v_fma_mix_f32 v155, v54, v128, v155 op_sel:[1,0,0] op_sel_hi:[1,0,0]
	v_fma_mix_f32 v156, v55, v128, v156 op_sel_hi:[1,0,0]
	v_fma_mix_f32 v157, v55, v128, v157 op_sel:[1,0,0] op_sel_hi:[1,0,0]
	v_fma_mix_f32 v154, v56, v129, v154 op_sel_hi:[1,0,0]
	v_fma_mix_f32 v155, v56, v129, v155 op_sel:[1,0,0] op_sel_hi:[1,0,0]
	v_fma_mix_f32 v156, v57, v129, v156 op_sel_hi:[1,0,0]
	v_fma_mix_f32 v157, v57, v129, v157 op_sel:[1,0,0] op_sel_hi:[1,0,0]
	v_fma_mix_f32 v154, v58, v130, v154 op_sel_hi:[1,0,0]
	v_fma_mix_f32 v155, v58, v130, v155 op_sel:[1,0,0] op_sel_hi:[1,0,0]
	v_fma_mix_f32 v156, v59, v130, v156 op_sel_hi:[1,0,0]
	v_fma_mix_f32 v157, v59, v130, v157 op_sel:[1,0,0] op_sel_hi:[1,0,0]
	v_fma_mix_f32 v154, v60, v131, v154 op_sel_hi:[1,0,0]
	v_fma_mix_f32 v155, v60, v131, v155 op_sel:[1,0,0] op_sel_hi:[1,0,0]
	v_fma_mix_f32 v156, v61, v131, v156 op_sel_hi:[1,0,0]
	v_fma_mix_f32 v157, v61, v131, v157 op_sel:[1,0,0] op_sel_hi:[1,0,0]
	v_fma_mix_f32 v154, v62, v132, v154 op_sel_hi:[1,0,0]
	v_fma_mix_f32 v155, v62, v132, v155 op_sel:[1,0,0] op_sel_hi:[1,0,0]
	v_fma_mix_f32 v156, v63, v132, v156 op_sel_hi:[1,0,0]
	v_fma_mix_f32 v157, v63, v132, v157 op_sel:[1,0,0] op_sel_hi:[1,0,0]
	v_fma_mix_f32 v154, v64, v133, v154 op_sel_hi:[1,0,0]
	v_fma_mix_f32 v155, v64, v133, v155 op_sel:[1,0,0] op_sel_hi:[1,0,0]
	v_fma_mix_f32 v156, v65, v133, v156 op_sel_hi:[1,0,0]
	v_fma_mix_f32 v157, v65, v133, v157 op_sel:[1,0,0] op_sel_hi:[1,0,0]
	v_fma_mix_f32 v154, v66, v134, v154 op_sel_hi:[1,0,0]
	v_fma_mix_f32 v155, v66, v134, v155 op_sel:[1,0,0] op_sel_hi:[1,0,0]
	v_fma_mix_f32 v156, v67, v134, v156 op_sel_hi:[1,0,0]
	v_fma_mix_f32 v157, v67, v134, v157 op_sel:[1,0,0] op_sel_hi:[1,0,0]
	v_fma_mix_f32 v154, v68, v135, v154 op_sel_hi:[1,0,0]
	v_fma_mix_f32 v155, v68, v135, v155 op_sel:[1,0,0] op_sel_hi:[1,0,0]
	v_fma_mix_f32 v156, v69, v135, v156 op_sel_hi:[1,0,0]
	v_fma_mix_f32 v157, v69, v135, v157 op_sel:[1,0,0] op_sel_hi:[1,0,0]
	v_fma_mix_f32 v154, v70, v136, v154 op_sel_hi:[1,0,0]
	v_fma_mix_f32 v155, v70, v136, v155 op_sel:[1,0,0] op_sel_hi:[1,0,0]
	v_fma_mix_f32 v156, v71, v136, v156 op_sel_hi:[1,0,0]
	v_fma_mix_f32 v157, v71, v136, v157 op_sel:[1,0,0] op_sel_hi:[1,0,0]
	v_fma_mix_f32 v154, v72, v137, v154 op_sel_hi:[1,0,0]
	v_fma_mix_f32 v155, v72, v137, v155 op_sel:[1,0,0] op_sel_hi:[1,0,0]
	v_fma_mix_f32 v156, v73, v137, v156 op_sel_hi:[1,0,0]
	v_fma_mix_f32 v157, v73, v137, v157 op_sel:[1,0,0] op_sel_hi:[1,0,0]
	v_fma_mix_f32 v154, v74, v138, v154 op_sel_hi:[1,0,0]
	v_fma_mix_f32 v155, v74, v138, v155 op_sel:[1,0,0] op_sel_hi:[1,0,0]
	v_fma_mix_f32 v156, v75, v138, v156 op_sel_hi:[1,0,0]
	v_fma_mix_f32 v157, v75, v138, v157 op_sel:[1,0,0] op_sel_hi:[1,0,0]
	v_fma_mix_f32 v154, v76, v139, v154 op_sel_hi:[1,0,0]
	v_fma_mix_f32 v155, v76, v139, v155 op_sel:[1,0,0] op_sel_hi:[1,0,0]
	v_fma_mix_f32 v156, v77, v139, v156 op_sel_hi:[1,0,0]
	v_fma_mix_f32 v157, v77, v139, v157 op_sel:[1,0,0] op_sel_hi:[1,0,0]
	v_fma_mix_f32 v154, v78, v140, v154 op_sel_hi:[1,0,0]
	v_fma_mix_f32 v155, v78, v140, v155 op_sel:[1,0,0] op_sel_hi:[1,0,0]
	v_fma_mix_f32 v156, v79, v140, v156 op_sel_hi:[1,0,0]
	v_fma_mix_f32 v157, v79, v140, v157 op_sel:[1,0,0] op_sel_hi:[1,0,0]
	v_fma_mix_f32 v154, v80, v141, v154 op_sel_hi:[1,0,0]
	v_fma_mix_f32 v155, v80, v141, v155 op_sel:[1,0,0] op_sel_hi:[1,0,0]
	v_fma_mix_f32 v156, v81, v141, v156 op_sel_hi:[1,0,0]
	v_fma_mix_f32 v157, v81, v141, v157 op_sel:[1,0,0] op_sel_hi:[1,0,0]
	v_fma_mix_f32 v154, v82, v142, v154 op_sel_hi:[1,0,0]
	v_fma_mix_f32 v155, v82, v142, v155 op_sel:[1,0,0] op_sel_hi:[1,0,0]
	v_fma_mix_f32 v156, v83, v142, v156 op_sel_hi:[1,0,0]
	v_fma_mix_f32 v157, v83, v142, v157 op_sel:[1,0,0] op_sel_hi:[1,0,0]
	v_fma_mix_f32 v154, v84, v143, v154 op_sel_hi:[1,0,0]
	v_fma_mix_f32 v155, v84, v143, v155 op_sel:[1,0,0] op_sel_hi:[1,0,0]
	v_fma_mix_f32 v156, v85, v143, v156 op_sel_hi:[1,0,0]
	v_fma_mix_f32 v157, v85, v143, v157 op_sel:[1,0,0] op_sel_hi:[1,0,0]
	v_fma_mix_f32 v154, v86, v144, v154 op_sel_hi:[1,0,0]
	v_fma_mix_f32 v155, v86, v144, v155 op_sel:[1,0,0] op_sel_hi:[1,0,0]
	v_fma_mix_f32 v156, v87, v144, v156 op_sel_hi:[1,0,0]
	v_fma_mix_f32 v157, v87, v144, v157 op_sel:[1,0,0] op_sel_hi:[1,0,0]
	v_fma_mix_f32 v154, v88, v145, v154 op_sel_hi:[1,0,0]
	v_fma_mix_f32 v155, v88, v145, v155 op_sel:[1,0,0] op_sel_hi:[1,0,0]
	v_fma_mix_f32 v156, v89, v145, v156 op_sel_hi:[1,0,0]
	v_fma_mix_f32 v157, v89, v145, v157 op_sel:[1,0,0] op_sel_hi:[1,0,0]
	v_fma_mix_f32 v154, v90, v146, v154 op_sel_hi:[1,0,0]
	v_fma_mix_f32 v155, v90, v146, v155 op_sel:[1,0,0] op_sel_hi:[1,0,0]
	v_fma_mix_f32 v156, v91, v146, v156 op_sel_hi:[1,0,0]
	v_fma_mix_f32 v157, v91, v146, v157 op_sel:[1,0,0] op_sel_hi:[1,0,0]
	v_fma_mix_f32 v154, v92, v147, v154 op_sel_hi:[1,0,0]
	v_fma_mix_f32 v155, v92, v147, v155 op_sel:[1,0,0] op_sel_hi:[1,0,0]
	v_fma_mix_f32 v156, v93, v147, v156 op_sel_hi:[1,0,0]
	v_fma_mix_f32 v157, v93, v147, v157 op_sel:[1,0,0] op_sel_hi:[1,0,0]
	v_fma_mix_f32 v154, v94, v148, v154 op_sel_hi:[1,0,0]
	v_fma_mix_f32 v155, v94, v148, v155 op_sel:[1,0,0] op_sel_hi:[1,0,0]
	v_fma_mix_f32 v156, v95, v148, v156 op_sel_hi:[1,0,0]
	v_fma_mix_f32 v157, v95, v148, v157 op_sel:[1,0,0] op_sel_hi:[1,0,0]
	v_fma_mix_f32 v154, v96, v149, v154 op_sel_hi:[1,0,0]
	v_fma_mix_f32 v155, v96, v149, v155 op_sel:[1,0,0] op_sel_hi:[1,0,0]
	v_fma_mix_f32 v156, v97, v149, v156 op_sel_hi:[1,0,0]
	v_fma_mix_f32 v157, v97, v149, v157 op_sel:[1,0,0] op_sel_hi:[1,0,0]
	v_fma_mix_f32 v154, v98, v150, v154 op_sel_hi:[1,0,0]
	v_fma_mix_f32 v155, v98, v150, v155 op_sel:[1,0,0] op_sel_hi:[1,0,0]
	v_fma_mix_f32 v156, v99, v150, v156 op_sel_hi:[1,0,0]
	v_fma_mix_f32 v157, v99, v150, v157 op_sel:[1,0,0] op_sel_hi:[1,0,0]
	v_fma_mix_f32 v154, v100, v151, v154 op_sel_hi:[1,0,0]
	v_fma_mix_f32 v155, v100, v151, v155 op_sel:[1,0,0] op_sel_hi:[1,0,0]
	v_fma_mix_f32 v156, v101, v151, v156 op_sel_hi:[1,0,0]
	v_fma_mix_f32 v157, v101, v151, v157 op_sel:[1,0,0] op_sel_hi:[1,0,0]
	global_store_dwordx4 v222, v[154:157], s[8:9]
	s_endpgm
